# speedup vs baseline: 1.0023x; 1.0023x over previous
.Lou_loop:
	s_waitcnt lgkmcnt(0)
	v_mfma_f32_16x16x32_bf16 v[64:67], v[176:179], v[160:163], v[64:67]
	ds_read_b128 v[200:203], v11 offset:0
	v_mfma_f32_16x16x32_bf16 v[68:71], v[176:179], v[164:167], v[68:71]
	s_add_u32 m0, s20, 0x5000
	v_mfma_f32_16x16x32_bf16 v[72:75], v[176:179], v[168:171], v[72:75]
	ds_read_b128 v[204:207], v11 offset:2048
	v_mfma_f32_16x16x32_bf16 v[76:79], v[176:179], v[172:175], v[76:79]
	global_load_lds_dwordx4 v3, s[18:19]
	v_mfma_f32_16x16x32_bf16 v[80:83], v[180:183], v[160:163], v[80:83]
	ds_read_b128 v[208:211], v11 offset:4096
	v_mfma_f32_16x16x32_bf16 v[84:87], v[180:183], v[164:167], v[84:87]
	s_add_u32 m0, s20, 0x6000
	v_mfma_f32_16x16x32_bf16 v[88:91], v[180:183], v[168:171], v[88:91]
	ds_read_b128 v[212:215], v11 offset:6144
	v_mfma_f32_16x16x32_bf16 v[92:95], v[180:183], v[172:175], v[92:95]
	global_load_lds_dwordx4 v4, s[18:19]
	v_mfma_f32_16x16x32_bf16 v[96:99], v[184:187], v[160:163], v[96:99]
	ds_read_b128 v[216:219], v13 offset:0
	v_mfma_f32_16x16x32_bf16 v[100:103], v[184:187], v[164:167], v[100:103]
	s_add_u32 m0, s20, 0x7000
	v_mfma_f32_16x16x32_bf16 v[104:107], v[184:187], v[168:171], v[104:107]
	ds_read_b128 v[220:223], v13 offset:2048
	v_mfma_f32_16x16x32_bf16 v[108:111], v[184:187], v[172:175], v[108:111]
	global_load_lds_dwordx4 v5, s[18:19]
	v_mfma_f32_16x16x32_bf16 v[112:115], v[188:191], v[160:163], v[112:115]
	ds_read_b128 v[224:227], v13 offset:4096
	v_mfma_f32_16x16x32_bf16 v[116:119], v[188:191], v[164:167], v[116:119]
	s_add_u32 m0, s20, 0x8000
	v_mfma_f32_16x16x32_bf16 v[120:123], v[188:191], v[168:171], v[120:123]
	ds_read_b128 v[228:231], v13 offset:6144
	v_mfma_f32_16x16x32_bf16 v[124:127], v[188:191], v[172:175], v[124:127]
	global_load_lds_dwordx4 v6, s[18:19]
	v_mfma_f32_16x16x32_bf16 v[128:131], v[192:195], v[160:163], v[128:131]
	ds_read_b128 v[232:235], v13 offset:8192
	v_mfma_f32_16x16x32_bf16 v[132:135], v[192:195], v[164:167], v[132:135]
	s_add_u32 m0, s20, 0x9000
	v_mfma_f32_16x16x32_bf16 v[136:139], v[192:195], v[168:171], v[136:139]
	ds_read_b128 v[236:239], v13 offset:10240
	v_mfma_f32_16x16x32_bf16 v[140:143], v[192:195], v[172:175], v[140:143]
	global_load_lds_dwordx4 v7, s[18:19]
	v_mfma_f32_16x16x32_bf16 v[144:147], v[196:199], v[160:163], v[144:147]
	s_add_u32 s16, s16, 0x80
	s_addc_u32 s17, s17, 0
	s_add_u32 s18, s18, 0x80
	s_addc_u32 s19, s19, 0
	v_mfma_f32_16x16x32_bf16 v[148:151], v[196:199], v[164:167], v[148:151]
	s_add_u32 s20, s20, 0xa000
	s_sub_u32 s22, s20, 0x28000
	s_cmp_ge_u32 s20, 0x28000
	s_cselect_b32 s20, s22, s20
	v_mfma_f32_16x16x32_bf16 v[152:155], v[196:199], v[168:171], v[152:155]
	v_add_u32_e32 v10, s21, v8
	v_add_u32_e32 v12, s21, v9
	v_xor_b32_e32 v11, 64, v10
	v_xor_b32_e32 v13, 64, v12
	v_mfma_f32_16x16x32_bf16 v[156:159], v[196:199], v[172:175], v[156:159]
	s_add_u32 s21, s21, 0xa000
	s_sub_u32 s23, s21, 0x28000
	s_cmp_ge_u32 s21, 0x28000
	s_cselect_b32 s21, s23, s21
	s_waitcnt lgkmcnt(0)
	v_mfma_f32_16x16x32_bf16 v[64:67], v[216:219], v[200:203], v[64:67]
	v_mfma_f32_16x16x32_bf16 v[68:71], v[216:219], v[204:207], v[68:71]
	v_mfma_f32_16x16x32_bf16 v[72:75], v[216:219], v[208:211], v[72:75]
	v_mfma_f32_16x16x32_bf16 v[76:79], v[216:219], v[212:215], v[76:79]
	s_waitcnt vmcnt(20)
	s_barrier
	v_mfma_f32_16x16x32_bf16 v[80:83], v[220:223], v[200:203], v[80:83]
	ds_read_b128 v[160:163], v10 offset:0
	v_mfma_f32_16x16x32_bf16 v[84:87], v[220:223], v[204:207], v[84:87]
	s_add_u32 m0, s20, 0x0
	v_mfma_f32_16x16x32_bf16 v[88:91], v[220:223], v[208:211], v[88:91]
	ds_read_b128 v[164:167], v10 offset:2048
	v_mfma_f32_16x16x32_bf16 v[92:95], v[220:223], v[212:215], v[92:95]
	global_load_lds_dwordx4 v2, s[16:17]
	v_mfma_f32_16x16x32_bf16 v[96:99], v[224:227], v[200:203], v[96:99]
	ds_read_b128 v[168:171], v10 offset:4096
	v_mfma_f32_16x16x32_bf16 v[100:103], v[224:227], v[204:207], v[100:103]
	s_add_u32 m0, s20, 0x1000
	v_mfma_f32_16x16x32_bf16 v[104:107], v[224:227], v[208:211], v[104:107]
	ds_read_b128 v[172:175], v10 offset:6144
	v_mfma_f32_16x16x32_bf16 v[108:111], v[224:227], v[212:215], v[108:111]
	global_load_lds_dwordx4 v3, s[16:17]
	v_mfma_f32_16x16x32_bf16 v[112:115], v[228:231], v[200:203], v[112:115]
	ds_read_b128 v[176:179], v12 offset:0
	v_mfma_f32_16x16x32_bf16 v[116:119], v[228:231], v[204:207], v[116:119]
	s_add_u32 m0, s20, 0x2000
	v_mfma_f32_16x16x32_bf16 v[120:123], v[228:231], v[208:211], v[120:123]
	ds_read_b128 v[180:183], v12 offset:2048
	v_mfma_f32_16x16x32_bf16 v[124:127], v[228:231], v[212:215], v[124:127]
	global_load_lds_dwordx4 v4, s[16:17]
	v_mfma_f32_16x16x32_bf16 v[128:131], v[232:235], v[200:203], v[128:131]
	ds_read_b128 v[184:187], v12 offset:4096
	v_mfma_f32_16x16x32_bf16 v[132:135], v[232:235], v[204:207], v[132:135]
	s_add_u32 m0, s20, 0x3000
	v_mfma_f32_16x16x32_bf16 v[136:139], v[232:235], v[208:211], v[136:139]
	ds_read_b128 v[188:191], v12 offset:6144
	v_mfma_f32_16x16x32_bf16 v[140:143], v[232:235], v[212:215], v[140:143]
	global_load_lds_dwordx4 v5, s[16:17]
	v_mfma_f32_16x16x32_bf16 v[144:147], v[236:239], v[200:203], v[144:147]
	ds_read_b128 v[192:195], v12 offset:8192
	v_mfma_f32_16x16x32_bf16 v[148:151], v[236:239], v[204:207], v[148:151]
	s_add_u32 m0, s20, 0x4000
	v_mfma_f32_16x16x32_bf16 v[152:155], v[236:239], v[208:211], v[152:155]
	ds_read_b128 v[196:199], v12 offset:10240
	v_mfma_f32_16x16x32_bf16 v[156:159], v[236:239], v[212:215], v[156:159]
	global_load_lds_dwordx4 v2, s[18:19]
	s_add_u32 s15, s15, 1
	s_cmp_lt_u32 s15, 8
	s_cbranch_scc1 .Lou_loop
	s_waitcnt lgkmcnt(0)
	v_mfma_f32_16x16x32_bf16 v[64:67], v[176:179], v[160:163], v[64:67]
	ds_read_b128 v[200:203], v11 offset:0
	v_mfma_f32_16x16x32_bf16 v[68:71], v[176:179], v[164:167], v[68:71]
	s_add_u32 m0, s20, 0x5000
	v_mfma_f32_16x16x32_bf16 v[72:75], v[176:179], v[168:171], v[72:75]
	ds_read_b128 v[204:207], v11 offset:2048
	v_mfma_f32_16x16x32_bf16 v[76:79], v[176:179], v[172:175], v[76:79]
	global_load_lds_dwordx4 v3, s[18:19]
	v_mfma_f32_16x16x32_bf16 v[80:83], v[180:183], v[160:163], v[80:83]
	ds_read_b128 v[208:211], v11 offset:4096
	v_mfma_f32_16x16x32_bf16 v[84:87], v[180:183], v[164:167], v[84:87]
	s_add_u32 m0, s20, 0x6000
	v_mfma_f32_16x16x32_bf16 v[88:91], v[180:183], v[168:171], v[88:91]
	ds_read_b128 v[212:215], v11 offset:6144
	v_mfma_f32_16x16x32_bf16 v[92:95], v[180:183], v[172:175], v[92:95]
	global_load_lds_dwordx4 v4, s[18:19]
	v_mfma_f32_16x16x32_bf16 v[96:99], v[184:187], v[160:163], v[96:99]
	ds_read_b128 v[216:219], v13 offset:0
	v_mfma_f32_16x16x32_bf16 v[100:103], v[184:187], v[164:167], v[100:103]
	s_add_u32 m0, s20, 0x7000
	v_mfma_f32_16x16x32_bf16 v[104:107], v[184:187], v[168:171], v[104:107]
	ds_read_b128 v[220:223], v13 offset:2048
	v_mfma_f32_16x16x32_bf16 v[108:111], v[184:187], v[172:175], v[108:111]
	global_load_lds_dwordx4 v5, s[18:19]
	v_mfma_f32_16x16x32_bf16 v[112:115], v[188:191], v[160:163], v[112:115]
	ds_read_b128 v[224:227], v13 offset:4096
	v_mfma_f32_16x16x32_bf16 v[116:119], v[188:191], v[164:167], v[116:119]
	s_add_u32 m0, s20, 0x8000
	v_mfma_f32_16x16x32_bf16 v[120:123], v[188:191], v[168:171], v[120:123]
	ds_read_b128 v[228:231], v13 offset:6144
	v_mfma_f32_16x16x32_bf16 v[124:127], v[188:191], v[172:175], v[124:127]
	global_load_lds_dwordx4 v6, s[18:19]
	v_mfma_f32_16x16x32_bf16 v[128:131], v[192:195], v[160:163], v[128:131]
	ds_read_b128 v[232:235], v13 offset:8192
	v_mfma_f32_16x16x32_bf16 v[132:135], v[192:195], v[164:167], v[132:135]
	s_add_u32 m0, s20, 0x9000
	v_mfma_f32_16x16x32_bf16 v[136:139], v[192:195], v[168:171], v[136:139]
	ds_read_b128 v[236:239], v13 offset:10240
	v_mfma_f32_16x16x32_bf16 v[140:143], v[192:195], v[172:175], v[140:143]
	global_load_lds_dwordx4 v7, s[18:19]
	v_mfma_f32_16x16x32_bf16 v[144:147], v[196:199], v[160:163], v[144:147]
	s_add_u32 s16, s16, 0x80
	s_addc_u32 s17, s17, 0
	s_add_u32 s18, s18, 0x80
	s_addc_u32 s19, s19, 0
	v_mfma_f32_16x16x32_bf16 v[148:151], v[196:199], v[164:167], v[148:151]
	s_add_u32 s20, s20, 0xa000
	s_sub_u32 s22, s20, 0x28000
	s_cmp_ge_u32 s20, 0x28000
	s_cselect_b32 s20, s22, s20
	v_mfma_f32_16x16x32_bf16 v[152:155], v[196:199], v[168:171], v[152:155]
	v_add_u32_e32 v10, s21, v8
	v_add_u32_e32 v12, s21, v9
	v_xor_b32_e32 v11, 64, v10
	v_xor_b32_e32 v13, 64, v12
	v_mfma_f32_16x16x32_bf16 v[156:159], v[196:199], v[172:175], v[156:159]
	s_add_u32 s21, s21, 0xa000
	s_sub_u32 s23, s21, 0x28000
	s_cmp_ge_u32 s21, 0x28000
	s_cselect_b32 s21, s23, s21
	s_waitcnt lgkmcnt(0)
	v_mfma_f32_16x16x32_bf16 v[64:67], v[216:219], v[200:203], v[64:67]
	v_mfma_f32_16x16x32_bf16 v[68:71], v[216:219], v[204:207], v[68:71]
	v_mfma_f32_16x16x32_bf16 v[72:75], v[216:219], v[208:211], v[72:75]
	v_mfma_f32_16x16x32_bf16 v[76:79], v[216:219], v[212:215], v[76:79]
	s_waitcnt vmcnt(20)
	s_barrier
	v_mfma_f32_16x16x32_bf16 v[80:83], v[220:223], v[200:203], v[80:83]
	ds_read_b128 v[160:163], v10 offset:0
	v_mfma_f32_16x16x32_bf16 v[84:87], v[220:223], v[204:207], v[84:87]
	global_load_dwordx4 v[16:19], v56, s[8:9] offset:0
	v_mfma_f32_16x16x32_bf16 v[88:91], v[220:223], v[208:211], v[88:91]
	ds_read_b128 v[164:167], v10 offset:2048
	v_mfma_f32_16x16x32_bf16 v[92:95], v[220:223], v[212:215], v[92:95]
	global_load_dwordx4 v[20:23], v57, s[8:9] offset:0
	v_mfma_f32_16x16x32_bf16 v[96:99], v[224:227], v[200:203], v[96:99]
	ds_read_b128 v[168:171], v10 offset:4096
	v_mfma_f32_16x16x32_bf16 v[100:103], v[224:227], v[204:207], v[100:103]
	global_load_dwordx4 v[24:27], v58, s[8:9] offset:0
	v_mfma_f32_16x16x32_bf16 v[104:107], v[224:227], v[208:211], v[104:107]
	ds_read_b128 v[172:175], v10 offset:6144
	v_mfma_f32_16x16x32_bf16 v[108:111], v[224:227], v[212:215], v[108:111]
	global_load_dwordx4 v[28:31], v59, s[8:9] offset:0
	v_mfma_f32_16x16x32_bf16 v[112:115], v[228:231], v[200:203], v[112:115]
	ds_read_b128 v[176:179], v12 offset:0
	v_mfma_f32_16x16x32_bf16 v[116:119], v[228:231], v[204:207], v[116:119]
	global_load_dwordx4 v[32:35], v56, s[8:9] offset:64
	v_mfma_f32_16x16x32_bf16 v[120:123], v[228:231], v[208:211], v[120:123]
	ds_read_b128 v[180:183], v12 offset:2048
	v_mfma_f32_16x16x32_bf16 v[124:127], v[228:231], v[212:215], v[124:127]
	global_load_dwordx4 v[36:39], v57, s[8:9] offset:64
	v_mfma_f32_16x16x32_bf16 v[128:131], v[232:235], v[200:203], v[128:131]
	ds_read_b128 v[184:187], v12 offset:4096
	v_mfma_f32_16x16x32_bf16 v[132:135], v[232:235], v[204:207], v[132:135]
	global_load_dwordx4 v[40:43], v58, s[8:9] offset:64
	v_mfma_f32_16x16x32_bf16 v[136:139], v[232:235], v[208:211], v[136:139]
	ds_read_b128 v[188:191], v12 offset:6144
	v_mfma_f32_16x16x32_bf16 v[140:143], v[232:235], v[212:215], v[140:143]
	global_load_dwordx4 v[44:47], v59, s[8:9] offset:64
	v_mfma_f32_16x16x32_bf16 v[144:147], v[236:239], v[200:203], v[144:147]
	ds_read_b128 v[192:195], v12 offset:8192
	v_mfma_f32_16x16x32_bf16 v[148:151], v[236:239], v[204:207], v[148:151]
	global_load_dwordx4 v[48:51], v56, s[8:9] offset:128
	v_mfma_f32_16x16x32_bf16 v[152:155], v[236:239], v[208:211], v[152:155]
	ds_read_b128 v[196:199], v12 offset:10240
	v_mfma_f32_16x16x32_bf16 v[156:159], v[236:239], v[212:215], v[156:159]
	global_load_dwordx4 v[52:55], v57, s[8:9] offset:128
	global_load_dwordx4 v[240:243], v58, s[8:9] offset:128
	global_load_dwordx4 v[244:247], v59, s[8:9] offset:128
	global_load_dwordx4 v[248:251], v56, s[8:9] offset:192
	global_load_dwordx4 v[252:255], v57, s[8:9] offset:192
	s_waitcnt lgkmcnt(0)
	v_mfma_f32_16x16x32_bf16 v[64:67], v[176:179], v[160:163], v[64:67]
	ds_read_b128 v[200:203], v11 offset:0
	v_mfma_f32_16x16x32_bf16 v[68:71], v[176:179], v[164:167], v[68:71]
	ds_read_b128 v[204:207], v11 offset:2048
	v_mfma_f32_16x16x32_bf16 v[72:75], v[176:179], v[168:171], v[72:75]
	ds_read_b128 v[208:211], v11 offset:4096
	v_mfma_f32_16x16x32_bf16 v[76:79], v[176:179], v[172:175], v[76:79]
	ds_read_b128 v[212:215], v11 offset:6144
	v_mfma_f32_16x16x32_bf16 v[80:83], v[180:183], v[160:163], v[80:83]
	ds_read_b128 v[216:219], v13 offset:0
	v_mfma_f32_16x16x32_bf16 v[84:87], v[180:183], v[164:167], v[84:87]
	ds_read_b128 v[220:223], v13 offset:2048
	v_mfma_f32_16x16x32_bf16 v[88:91], v[180:183], v[168:171], v[88:91]
	ds_read_b128 v[224:227], v13 offset:4096
	v_mfma_f32_16x16x32_bf16 v[92:95], v[180:183], v[172:175], v[92:95]
	ds_read_b128 v[228:231], v13 offset:6144
	v_mfma_f32_16x16x32_bf16 v[96:99], v[184:187], v[160:163], v[96:99]
	ds_read_b128 v[232:235], v13 offset:8192
	v_mfma_f32_16x16x32_bf16 v[100:103], v[184:187], v[164:167], v[100:103]
	ds_read_b128 v[236:239], v13 offset:10240
	v_mfma_f32_16x16x32_bf16 v[104:107], v[184:187], v[168:171], v[104:107]
	v_mfma_f32_16x16x32_bf16 v[108:111], v[184:187], v[172:175], v[108:111]
	v_mfma_f32_16x16x32_bf16 v[112:115], v[188:191], v[160:163], v[112:115]
	v_mfma_f32_16x16x32_bf16 v[116:119], v[188:191], v[164:167], v[116:119]
	v_mfma_f32_16x16x32_bf16 v[120:123], v[188:191], v[168:171], v[120:123]
	v_mfma_f32_16x16x32_bf16 v[124:127], v[188:191], v[172:175], v[124:127]
	v_mfma_f32_16x16x32_bf16 v[128:131], v[192:195], v[160:163], v[128:131]
	v_mfma_f32_16x16x32_bf16 v[132:135], v[192:195], v[164:167], v[132:135]
	v_mfma_f32_16x16x32_bf16 v[136:139], v[192:195], v[168:171], v[136:139]
	v_mfma_f32_16x16x32_bf16 v[140:143], v[192:195], v[172:175], v[140:143]
	v_mfma_f32_16x16x32_bf16 v[144:147], v[196:199], v[160:163], v[144:147]
	v_add_u32_e32 v10, s21, v8
	v_add_u32_e32 v12, s21, v9
	v_xor_b32_e32 v11, 64, v10
	v_xor_b32_e32 v13, 64, v12
	v_mfma_f32_16x16x32_bf16 v[148:151], v[196:199], v[164:167], v[148:151]
	s_add_u32 s21, s21, 0xa000
	s_sub_u32 s23, s21, 0x28000
	s_cmp_ge_u32 s21, 0x28000
	s_cselect_b32 s21, s23, s21
	v_mfma_f32_16x16x32_bf16 v[152:155], v[196:199], v[168:171], v[152:155]
	v_mfma_f32_16x16x32_bf16 v[156:159], v[196:199], v[172:175], v[156:159]
	s_waitcnt lgkmcnt(0)
	v_mfma_f32_16x16x32_bf16 v[64:67], v[216:219], v[200:203], v[64:67]
	v_mfma_f32_16x16x32_bf16 v[68:71], v[216:219], v[204:207], v[68:71]
	v_mfma_f32_16x16x32_bf16 v[72:75], v[216:219], v[208:211], v[72:75]
	v_mfma_f32_16x16x32_bf16 v[76:79], v[216:219], v[212:215], v[76:79]
	s_waitcnt vmcnt(24)
	s_barrier
	v_mfma_f32_16x16x32_bf16 v[80:83], v[220:223], v[200:203], v[80:83]
	ds_read_b128 v[160:163], v10 offset:0
	v_mfma_f32_16x16x32_bf16 v[84:87], v[220:223], v[204:207], v[84:87]
	ds_read_b128 v[164:167], v10 offset:2048
	v_mfma_f32_16x16x32_bf16 v[88:91], v[220:223], v[208:211], v[88:91]
	ds_read_b128 v[168:171], v10 offset:4096
	v_mfma_f32_16x16x32_bf16 v[92:95], v[220:223], v[212:215], v[92:95]
	ds_read_b128 v[172:175], v10 offset:6144
	v_mfma_f32_16x16x32_bf16 v[96:99], v[224:227], v[200:203], v[96:99]
	ds_read_b128 v[176:179], v12 offset:0
	v_mfma_f32_16x16x32_bf16 v[100:103], v[224:227], v[204:207], v[100:103]
	ds_read_b128 v[180:183], v12 offset:2048
	v_mfma_f32_16x16x32_bf16 v[104:107], v[224:227], v[208:211], v[104:107]
	ds_read_b128 v[184:187], v12 offset:4096
	v_mfma_f32_16x16x32_bf16 v[108:111], v[224:227], v[212:215], v[108:111]
	ds_read_b128 v[188:191], v12 offset:6144
	v_mfma_f32_16x16x32_bf16 v[112:115], v[228:231], v[200:203], v[112:115]
	ds_read_b128 v[192:195], v12 offset:8192
	v_mfma_f32_16x16x32_bf16 v[116:119], v[228:231], v[204:207], v[116:119]
	ds_read_b128 v[196:199], v12 offset:10240
	v_mfma_f32_16x16x32_bf16 v[120:123], v[228:231], v[208:211], v[120:123]
	v_mfma_f32_16x16x32_bf16 v[124:127], v[228:231], v[212:215], v[124:127]
	v_mfma_f32_16x16x32_bf16 v[128:131], v[232:235], v[200:203], v[128:131]
	v_mfma_f32_16x16x32_bf16 v[132:135], v[232:235], v[204:207], v[132:135]
	v_mfma_f32_16x16x32_bf16 v[136:139], v[232:235], v[208:211], v[136:139]
	v_mfma_f32_16x16x32_bf16 v[140:143], v[232:235], v[212:215], v[140:143]
	v_mfma_f32_16x16x32_bf16 v[144:147], v[236:239], v[200:203], v[144:147]
	v_mfma_f32_16x16x32_bf16 v[148:151], v[236:239], v[204:207], v[148:151]
	v_mfma_f32_16x16x32_bf16 v[152:155], v[236:239], v[208:211], v[152:155]
	v_mfma_f32_16x16x32_bf16 v[156:159], v[236:239], v[212:215], v[156:159]
	s_waitcnt lgkmcnt(0)
	v_mfma_f32_16x16x32_bf16 v[64:67], v[176:179], v[160:163], v[64:67]
	ds_read_b128 v[200:203], v11 offset:0
	v_mfma_f32_16x16x32_bf16 v[68:71], v[176:179], v[164:167], v[68:71]
	ds_read_b128 v[204:207], v11 offset:2048
	v_mfma_f32_16x16x32_bf16 v[72:75], v[176:179], v[168:171], v[72:75]
	ds_read_b128 v[208:211], v11 offset:4096
	v_mfma_f32_16x16x32_bf16 v[76:79], v[176:179], v[172:175], v[76:79]
	ds_read_b128 v[212:215], v11 offset:6144
	v_mfma_f32_16x16x32_bf16 v[80:83], v[180:183], v[160:163], v[80:83]
	ds_read_b128 v[216:219], v13 offset:0
	v_mfma_f32_16x16x32_bf16 v[84:87], v[180:183], v[164:167], v[84:87]
	ds_read_b128 v[220:223], v13 offset:2048
	v_mfma_f32_16x16x32_bf16 v[88:91], v[180:183], v[168:171], v[88:91]
	ds_read_b128 v[224:227], v13 offset:4096
	v_mfma_f32_16x16x32_bf16 v[92:95], v[180:183], v[172:175], v[92:95]
	ds_read_b128 v[228:231], v13 offset:6144
	v_mfma_f32_16x16x32_bf16 v[96:99], v[184:187], v[160:163], v[96:99]
	ds_read_b128 v[232:235], v13 offset:8192
	v_mfma_f32_16x16x32_bf16 v[100:103], v[184:187], v[164:167], v[100:103]
	ds_read_b128 v[236:239], v13 offset:10240
	v_mfma_f32_16x16x32_bf16 v[104:107], v[184:187], v[168:171], v[104:107]
	v_mfma_f32_16x16x32_bf16 v[108:111], v[184:187], v[172:175], v[108:111]
	v_mfma_f32_16x16x32_bf16 v[112:115], v[188:191], v[160:163], v[112:115]
	v_mfma_f32_16x16x32_bf16 v[116:119], v[188:191], v[164:167], v[116:119]
	v_mfma_f32_16x16x32_bf16 v[120:123], v[188:191], v[168:171], v[120:123]
	v_mfma_f32_16x16x32_bf16 v[124:127], v[188:191], v[172:175], v[124:127]
	v_mfma_f32_16x16x32_bf16 v[128:131], v[192:195], v[160:163], v[128:131]
	v_mfma_f32_16x16x32_bf16 v[132:135], v[192:195], v[164:167], v[132:135]
	v_mfma_f32_16x16x32_bf16 v[136:139], v[192:195], v[168:171], v[136:139]
	v_mfma_f32_16x16x32_bf16 v[140:143], v[192:195], v[172:175], v[140:143]
	v_mfma_f32_16x16x32_bf16 v[144:147], v[196:199], v[160:163], v[144:147]
	v_add_u32_e32 v10, s21, v8
	v_add_u32_e32 v12, s21, v9
	v_xor_b32_e32 v11, 64, v10
	v_xor_b32_e32 v13, 64, v12
	v_mfma_f32_16x16x32_bf16 v[148:151], v[196:199], v[164:167], v[148:151]
	s_add_u32 s21, s21, 0xa000
	s_sub_u32 s23, s21, 0x28000
	s_cmp_ge_u32 s21, 0x28000
	s_cselect_b32 s21, s23, s21
	v_mfma_f32_16x16x32_bf16 v[152:155], v[196:199], v[168:171], v[152:155]
	v_mfma_f32_16x16x32_bf16 v[156:159], v[196:199], v[172:175], v[156:159]
	s_waitcnt lgkmcnt(0)
	v_mfma_f32_16x16x32_bf16 v[64:67], v[216:219], v[200:203], v[64:67]
	v_mfma_f32_16x16x32_bf16 v[68:71], v[216:219], v[204:207], v[68:71]
	v_mfma_f32_16x16x32_bf16 v[72:75], v[216:219], v[208:211], v[72:75]
	v_mfma_f32_16x16x32_bf16 v[76:79], v[216:219], v[212:215], v[76:79]
	s_waitcnt vmcnt(14)
	s_barrier
	v_mfma_f32_16x16x32_bf16 v[80:83], v[220:223], v[200:203], v[80:83]
	ds_read_b128 v[160:163], v10 offset:0
	v_mfma_f32_16x16x32_bf16 v[84:87], v[220:223], v[204:207], v[84:87]
	ds_read_b128 v[164:167], v10 offset:2048
	v_mfma_f32_16x16x32_bf16 v[88:91], v[220:223], v[208:211], v[88:91]
	ds_read_b128 v[168:171], v10 offset:4096
	v_mfma_f32_16x16x32_bf16 v[92:95], v[220:223], v[212:215], v[92:95]
	ds_read_b128 v[172:175], v10 offset:6144
	v_mfma_f32_16x16x32_bf16 v[96:99], v[224:227], v[200:203], v[96:99]
	ds_read_b128 v[176:179], v12 offset:0
	v_mfma_f32_16x16x32_bf16 v[100:103], v[224:227], v[204:207], v[100:103]
	ds_read_b128 v[180:183], v12 offset:2048
	v_mfma_f32_16x16x32_bf16 v[104:107], v[224:227], v[208:211], v[104:107]
	ds_read_b128 v[184:187], v12 offset:4096
	v_mfma_f32_16x16x32_bf16 v[108:111], v[224:227], v[212:215], v[108:111]
	ds_read_b128 v[188:191], v12 offset:6144
	v_mfma_f32_16x16x32_bf16 v[112:115], v[228:231], v[200:203], v[112:115]
	ds_read_b128 v[192:195], v12 offset:8192
	v_mfma_f32_16x16x32_bf16 v[116:119], v[228:231], v[204:207], v[116:119]
	ds_read_b128 v[196:199], v12 offset:10240
	v_mfma_f32_16x16x32_bf16 v[120:123], v[228:231], v[208:211], v[120:123]
	v_mfma_f32_16x16x32_bf16 v[124:127], v[228:231], v[212:215], v[124:127]
	v_mfma_f32_16x16x32_bf16 v[128:131], v[232:235], v[200:203], v[128:131]
	v_mfma_f32_16x16x32_bf16 v[132:135], v[232:235], v[204:207], v[132:135]
	v_mfma_f32_16x16x32_bf16 v[136:139], v[232:235], v[208:211], v[136:139]
	v_mfma_f32_16x16x32_bf16 v[140:143], v[232:235], v[212:215], v[140:143]
	v_mfma_f32_16x16x32_bf16 v[144:147], v[236:239], v[200:203], v[144:147]
	v_mfma_f32_16x16x32_bf16 v[148:151], v[236:239], v[204:207], v[148:151]
	v_mfma_f32_16x16x32_bf16 v[152:155], v[236:239], v[208:211], v[152:155]
	v_mfma_f32_16x16x32_bf16 v[156:159], v[236:239], v[212:215], v[156:159]
	s_waitcnt lgkmcnt(0)
	v_mfma_f32_16x16x32_bf16 v[64:67], v[176:179], v[160:163], v[64:67]
	ds_read_b128 v[200:203], v11 offset:0
	v_mfma_f32_16x16x32_bf16 v[68:71], v[176:179], v[164:167], v[68:71]
	ds_read_b128 v[204:207], v11 offset:2048
	v_mfma_f32_16x16x32_bf16 v[72:75], v[176:179], v[168:171], v[72:75]
	ds_read_b128 v[208:211], v11 offset:4096
	v_mfma_f32_16x16x32_bf16 v[76:79], v[176:179], v[172:175], v[76:79]
	ds_read_b128 v[212:215], v11 offset:6144
	v_mfma_f32_16x16x32_bf16 v[80:83], v[180:183], v[160:163], v[80:83]
	ds_read_b128 v[216:219], v13 offset:0
	v_mfma_f32_16x16x32_bf16 v[84:87], v[180:183], v[164:167], v[84:87]
	ds_read_b128 v[220:223], v13 offset:2048
	v_mfma_f32_16x16x32_bf16 v[88:91], v[180:183], v[168:171], v[88:91]
	ds_read_b128 v[224:227], v13 offset:4096
	v_mfma_f32_16x16x32_bf16 v[92:95], v[180:183], v[172:175], v[92:95]
	ds_read_b128 v[228:231], v13 offset:6144
	v_mfma_f32_16x16x32_bf16 v[96:99], v[184:187], v[160:163], v[96:99]
	ds_read_b128 v[232:235], v13 offset:8192
	v_mfma_f32_16x16x32_bf16 v[100:103], v[184:187], v[164:167], v[100:103]
	ds_read_b128 v[236:239], v13 offset:10240
	v_mfma_f32_16x16x32_bf16 v[104:107], v[184:187], v[168:171], v[104:107]
	v_mfma_f32_16x16x32_bf16 v[108:111], v[184:187], v[172:175], v[108:111]
	v_mfma_f32_16x16x32_bf16 v[112:115], v[188:191], v[160:163], v[112:115]
	v_mfma_f32_16x16x32_bf16 v[116:119], v[188:191], v[164:167], v[116:119]
	v_mfma_f32_16x16x32_bf16 v[120:123], v[188:191], v[168:171], v[120:123]
	v_mfma_f32_16x16x32_bf16 v[124:127], v[188:191], v[172:175], v[124:127]
	v_mfma_f32_16x16x32_bf16 v[128:131], v[192:195], v[160:163], v[128:131]
	v_mfma_f32_16x16x32_bf16 v[132:135], v[192:195], v[164:167], v[132:135]
	v_mfma_f32_16x16x32_bf16 v[136:139], v[192:195], v[168:171], v[136:139]
	v_mfma_f32_16x16x32_bf16 v[140:143], v[192:195], v[172:175], v[140:143]
	v_mfma_f32_16x16x32_bf16 v[144:147], v[196:199], v[160:163], v[144:147]
	v_mfma_f32_16x16x32_bf16 v[148:151], v[196:199], v[164:167], v[148:151]
	v_mfma_f32_16x16x32_bf16 v[152:155], v[196:199], v[168:171], v[152:155]
	v_mfma_f32_16x16x32_bf16 v[156:159], v[196:199], v[172:175], v[156:159]
	s_waitcnt lgkmcnt(0)
	v_mfma_f32_16x16x32_bf16 v[64:67], v[216:219], v[200:203], v[64:67]
	v_mfma_f32_16x16x32_bf16 v[68:71], v[216:219], v[204:207], v[68:71]
	global_load_dwordx4 v[160:163], v58, s[8:9] offset:192
	v_mfma_f32_16x16x32_bf16 v[72:75], v[216:219], v[208:211], v[72:75]
	v_mfma_f32_16x16x32_bf16 v[76:79], v[216:219], v[212:215], v[76:79]
	global_load_dwordx4 v[164:167], v59, s[8:9] offset:192
	v_mfma_f32_16x16x32_bf16 v[80:83], v[220:223], v[200:203], v[80:83]
	v_mfma_f32_16x16x32_bf16 v[84:87], v[220:223], v[204:207], v[84:87]
	global_load_dwordx4 v[168:171], v56, s[8:9] offset:256
	v_mfma_f32_16x16x32_bf16 v[88:91], v[220:223], v[208:211], v[88:91]
	v_mfma_f32_16x16x32_bf16 v[92:95], v[220:223], v[212:215], v[92:95]
	global_load_dwordx4 v[172:175], v57, s[8:9] offset:256
	v_mfma_f32_16x16x32_bf16 v[96:99], v[224:227], v[200:203], v[96:99]
	v_mfma_f32_16x16x32_bf16 v[100:103], v[224:227], v[204:207], v[100:103]
	global_load_dwordx4 v[176:179], v58, s[8:9] offset:256
	v_mfma_f32_16x16x32_bf16 v[104:107], v[224:227], v[208:211], v[104:107]
	v_mfma_f32_16x16x32_bf16 v[108:111], v[224:227], v[212:215], v[108:111]
	global_load_dwordx4 v[180:183], v59, s[8:9] offset:256
	v_mfma_f32_16x16x32_bf16 v[112:115], v[228:231], v[200:203], v[112:115]
	v_mfma_f32_16x16x32_bf16 v[116:119], v[228:231], v[204:207], v[116:119]
	global_load_dwordx4 v[184:187], v56, s[8:9] offset:320
	v_mfma_f32_16x16x32_bf16 v[120:123], v[228:231], v[208:211], v[120:123]
	v_mfma_f32_16x16x32_bf16 v[124:127], v[228:231], v[212:215], v[124:127]
	global_load_dwordx4 v[188:191], v57, s[8:9] offset:320
	v_mfma_f32_16x16x32_bf16 v[128:131], v[232:235], v[200:203], v[128:131]
	v_mfma_f32_16x16x32_bf16 v[132:135], v[232:235], v[204:207], v[132:135]
	global_load_dwordx4 v[192:195], v58, s[8:9] offset:320
	v_mfma_f32_16x16x32_bf16 v[136:139], v[232:235], v[208:211], v[136:139]
	v_mfma_f32_16x16x32_bf16 v[140:143], v[232:235], v[212:215], v[140:143]
	global_load_dwordx4 v[196:199], v59, s[8:9] offset:320
	v_mfma_f32_16x16x32_bf16 v[144:147], v[236:239], v[200:203], v[144:147]
	v_mfma_f32_16x16x32_bf16 v[148:151], v[236:239], v[204:207], v[148:151]
	v_mfma_f32_16x16x32_bf16 v[152:155], v[236:239], v[208:211], v[152:155]
	v_mfma_f32_16x16x32_bf16 v[156:159], v[236:239], v[212:215], v[156:159]
	v_and_b32_e32 v12, 63, v0
	v_cmp_gt_u32_e32 vcc, 16, v12
	v_xor_b32_e32 v13, 16, v12
	v_lshlrev_b32_e32 v13, 2, v13
	v_xor_b32_e32 v12, 32, v12
	v_lshlrev_b32_e32 v12, 2, v12
	v_bfe_u32 v14, v0, 6, 1
	v_mul_u32_u24_e32 v14, 0x60, v14
	v_bfe_u32 v15, v0, 4, 2
	v_lshl_add_u32 v14, v15, 2, v14
	v_add_u32_e32 v14, s13, v14
	v_lshlrev_b32_e32 v14, 2, v14
	global_load_dwordx4 v[200:203], v14, s[24:25]
	global_load_dwordx4 v[204:207], v14, s[24:25] offset:64
	global_load_dwordx4 v[208:211], v14, s[24:25] offset:128
	global_load_dwordx4 v[212:215], v14, s[24:25] offset:192
	global_load_dwordx4 v[216:219], v14, s[24:25] offset:256
	global_load_dwordx4 v[220:223], v14, s[24:25] offset:320
	v_lshrrev_b32_e32 v60, 1, v56
	v_lshrrev_b32_e32 v61, 1, v57
	v_lshrrev_b32_e32 v62, 1, v58
	v_lshrrev_b32_e32 v63, 1, v59
	v_bfe_u32 v8, v0, 7, 1
	v_and_b32_e32 v9, 15, v0
	v_lshl_add_u32 v8, v8, 6, v9
	v_add_u32_e32 v8, s12, v8
	v_lshlrev_b32_e32 v8, 6, v8
	v_bfe_u32 v9, v0, 6, 1
	v_lshlrev_b32_e32 v9, 1, v9
	v_add_u32_e32 v9, s30, v9
	v_lshl_add_u32 v8, v9, 2, v8
	v_add_u32_e32 v9, 0x400, v8
	v_add_u32_e32 v10, 0x400, v9
	v_add_u32_e32 v11, 0x400, v10
	s_waitcnt vmcnt(0)
	v_pk_add_f32 v[64:65], v[64:65], v[16:17]
	v_pk_add_f32 v[66:67], v[66:67], v[18:19]
	global_store_dwordx4 v56, v[64:67], s[10:11]
	v_pk_mul_f32 v[224:225], v[200:201], v[64:65]
	v_pk_mul_f32 v[226:227], v[202:203], v[66:67]
	v_cvt_pk_bf16_f32 v228, v224, v225
	v_cvt_pk_bf16_f32 v229, v226, v227
	global_store_dwordx2 v60, v[228:229], s[28:29]
	v_pk_mul_f32 v[230:231], v[64:65], v[64:65]
	v_pk_mul_f32 v[232:233], v[66:67], v[66:67]
	v_add_f32_e32 v230, v230, v231
	v_add_f32_e32 v230, v232, v230
	v_add_f32_e32 v234, v233, v230
	v_pk_add_f32 v[80:81], v[80:81], v[32:33]
	v_pk_add_f32 v[82:83], v[82:83], v[34:35]
	global_store_dwordx4 v56, v[80:83], s[10:11] offset:64
	v_pk_mul_f32 v[224:225], v[204:205], v[80:81]
	v_pk_mul_f32 v[226:227], v[206:207], v[82:83]
	v_cvt_pk_bf16_f32 v228, v224, v225
	v_cvt_pk_bf16_f32 v229, v226, v227
	global_store_dwordx2 v60, v[228:229], s[28:29] offset:32
	v_pk_mul_f32 v[230:231], v[80:81], v[80:81]
	v_pk_mul_f32 v[232:233], v[82:83], v[82:83]
	v_add_f32_e32 v230, v230, v231
	v_add_f32_e32 v230, v232, v230
	v_add_f32_e32 v230, v233, v230
	v_add_f32_e32 v234, v234, v230
	v_pk_add_f32 v[96:97], v[96:97], v[48:49]
	v_pk_add_f32 v[98:99], v[98:99], v[50:51]
	global_store_dwordx4 v56, v[96:99], s[10:11] offset:128
	v_pk_mul_f32 v[224:225], v[208:209], v[96:97]
	v_pk_mul_f32 v[226:227], v[210:211], v[98:99]
	v_cvt_pk_bf16_f32 v228, v224, v225
	v_cvt_pk_bf16_f32 v229, v226, v227
	global_store_dwordx2 v60, v[228:229], s[28:29] offset:64
	v_pk_mul_f32 v[230:231], v[96:97], v[96:97]
	v_pk_mul_f32 v[232:233], v[98:99], v[98:99]
	v_add_f32_e32 v230, v230, v231
	v_add_f32_e32 v230, v232, v230
	v_add_f32_e32 v230, v233, v230
	v_add_f32_e32 v234, v234, v230
	v_pk_add_f32 v[112:113], v[112:113], v[248:249]
	v_pk_add_f32 v[114:115], v[114:115], v[250:251]
	global_store_dwordx4 v56, v[112:115], s[10:11] offset:192
	v_pk_mul_f32 v[224:225], v[212:213], v[112:113]
	v_pk_mul_f32 v[226:227], v[214:215], v[114:115]
	v_cvt_pk_bf16_f32 v228, v224, v225
	v_cvt_pk_bf16_f32 v229, v226, v227
	global_store_dwordx2 v60, v[228:229], s[28:29] offset:96
	v_pk_mul_f32 v[230:231], v[112:113], v[112:113]
	v_pk_mul_f32 v[232:233], v[114:115], v[114:115]
	v_add_f32_e32 v230, v230, v231
	v_add_f32_e32 v230, v232, v230
	v_add_f32_e32 v235, v233, v230
	v_pk_add_f32 v[128:129], v[128:129], v[168:169]
	v_pk_add_f32 v[130:131], v[130:131], v[170:171]
	global_store_dwordx4 v56, v[128:131], s[10:11] offset:256
	v_pk_mul_f32 v[224:225], v[216:217], v[128:129]
	v_pk_mul_f32 v[226:227], v[218:219], v[130:131]
	v_cvt_pk_bf16_f32 v228, v224, v225
	v_cvt_pk_bf16_f32 v229, v226, v227
	global_store_dwordx2 v60, v[228:229], s[28:29] offset:128
	v_pk_mul_f32 v[230:231], v[128:129], v[128:129]
	v_pk_mul_f32 v[232:233], v[130:131], v[130:131]
	v_add_f32_e32 v230, v230, v231
	v_add_f32_e32 v230, v232, v230
	v_add_f32_e32 v230, v233, v230
	v_add_f32_e32 v235, v235, v230
	v_pk_add_f32 v[144:145], v[144:145], v[184:185]
	v_pk_add_f32 v[146:147], v[146:147], v[186:187]
	global_store_dwordx4 v56, v[144:147], s[10:11] offset:320
	v_pk_mul_f32 v[224:225], v[220:221], v[144:145]
	v_pk_mul_f32 v[226:227], v[222:223], v[146:147]
	v_cvt_pk_bf16_f32 v228, v224, v225
	v_cvt_pk_bf16_f32 v229, v226, v227
	global_store_dwordx2 v60, v[228:229], s[28:29] offset:160
	v_pk_mul_f32 v[230:231], v[144:145], v[144:145]
	v_pk_mul_f32 v[232:233], v[146:147], v[146:147]
	v_add_f32_e32 v230, v230, v231
	v_add_f32_e32 v230, v232, v230
	v_add_f32_e32 v230, v233, v230
	v_add_f32_e32 v235, v235, v230
	v_pk_add_f32 v[68:69], v[68:69], v[20:21]
	v_pk_add_f32 v[70:71], v[70:71], v[22:23]
	global_store_dwordx4 v57, v[68:71], s[10:11]
	v_pk_mul_f32 v[224:225], v[200:201], v[68:69]
	v_pk_mul_f32 v[226:227], v[202:203], v[70:71]
	v_cvt_pk_bf16_f32 v228, v224, v225
	v_cvt_pk_bf16_f32 v229, v226, v227
	global_store_dwordx2 v61, v[228:229], s[28:29]
	v_pk_mul_f32 v[230:231], v[68:69], v[68:69]
	v_pk_mul_f32 v[232:233], v[70:71], v[70:71]
	v_add_f32_e32 v230, v230, v231
	v_add_f32_e32 v230, v232, v230
	v_add_f32_e32 v236, v233, v230
	v_pk_add_f32 v[84:85], v[84:85], v[36:37]
	v_pk_add_f32 v[86:87], v[86:87], v[38:39]
	global_store_dwordx4 v57, v[84:87], s[10:11] offset:64
	v_pk_mul_f32 v[224:225], v[204:205], v[84:85]
	v_pk_mul_f32 v[226:227], v[206:207], v[86:87]
	v_cvt_pk_bf16_f32 v228, v224, v225
	v_cvt_pk_bf16_f32 v229, v226, v227
	global_store_dwordx2 v61, v[228:229], s[28:29] offset:32
	v_pk_mul_f32 v[230:231], v[84:85], v[84:85]
	v_pk_mul_f32 v[232:233], v[86:87], v[86:87]
	v_add_f32_e32 v230, v230, v231
	v_add_f32_e32 v230, v232, v230
	v_add_f32_e32 v230, v233, v230
	v_add_f32_e32 v236, v236, v230
	v_pk_add_f32 v[100:101], v[100:101], v[52:53]
	v_pk_add_f32 v[102:103], v[102:103], v[54:55]
	global_store_dwordx4 v57, v[100:103], s[10:11] offset:128
	v_pk_mul_f32 v[224:225], v[208:209], v[100:101]
	v_pk_mul_f32 v[226:227], v[210:211], v[102:103]
	v_cvt_pk_bf16_f32 v228, v224, v225
	v_cvt_pk_bf16_f32 v229, v226, v227
	global_store_dwordx2 v61, v[228:229], s[28:29] offset:64
	v_pk_mul_f32 v[230:231], v[100:101], v[100:101]
	v_pk_mul_f32 v[232:233], v[102:103], v[102:103]
	v_add_f32_e32 v230, v230, v231
	v_add_f32_e32 v230, v232, v230
	v_add_f32_e32 v230, v233, v230
	v_add_f32_e32 v236, v236, v230
	v_pk_add_f32 v[116:117], v[116:117], v[252:253]
	v_pk_add_f32 v[118:119], v[118:119], v[254:255]
	global_store_dwordx4 v57, v[116:119], s[10:11] offset:192
	v_pk_mul_f32 v[224:225], v[212:213], v[116:117]
	v_pk_mul_f32 v[226:227], v[214:215], v[118:119]
	v_cvt_pk_bf16_f32 v228, v224, v225
	v_cvt_pk_bf16_f32 v229, v226, v227
	global_store_dwordx2 v61, v[228:229], s[28:29] offset:96
	v_pk_mul_f32 v[230:231], v[116:117], v[116:117]
	v_pk_mul_f32 v[232:233], v[118:119], v[118:119]
	v_add_f32_e32 v230, v230, v231
	v_add_f32_e32 v230, v232, v230
	v_add_f32_e32 v237, v233, v230
	v_pk_add_f32 v[132:133], v[132:133], v[172:173]
	v_pk_add_f32 v[134:135], v[134:135], v[174:175]
	global_store_dwordx4 v57, v[132:135], s[10:11] offset:256
	v_pk_mul_f32 v[224:225], v[216:217], v[132:133]
	v_pk_mul_f32 v[226:227], v[218:219], v[134:135]
	v_cvt_pk_bf16_f32 v228, v224, v225
	v_cvt_pk_bf16_f32 v229, v226, v227
	global_store_dwordx2 v61, v[228:229], s[28:29] offset:128
	v_pk_mul_f32 v[230:231], v[132:133], v[132:133]
	v_pk_mul_f32 v[232:233], v[134:135], v[134:135]
	v_add_f32_e32 v230, v230, v231
	v_add_f32_e32 v230, v232, v230
	v_add_f32_e32 v230, v233, v230
	v_add_f32_e32 v237, v237, v230
	v_pk_add_f32 v[148:149], v[148:149], v[188:189]
	v_pk_add_f32 v[150:151], v[150:151], v[190:191]
	global_store_dwordx4 v57, v[148:151], s[10:11] offset:320
	v_pk_mul_f32 v[224:225], v[220:221], v[148:149]
	v_pk_mul_f32 v[226:227], v[222:223], v[150:151]
	v_cvt_pk_bf16_f32 v228, v224, v225
	v_cvt_pk_bf16_f32 v229, v226, v227
	global_store_dwordx2 v61, v[228:229], s[28:29] offset:160
	v_pk_mul_f32 v[230:231], v[148:149], v[148:149]
	v_pk_mul_f32 v[232:233], v[150:151], v[150:151]
	v_add_f32_e32 v230, v230, v231
	v_add_f32_e32 v230, v232, v230
	v_add_f32_e32 v230, v233, v230
	v_add_f32_e32 v237, v237, v230
	v_pk_add_f32 v[72:73], v[72:73], v[24:25]
	v_pk_add_f32 v[74:75], v[74:75], v[26:27]
	global_store_dwordx4 v58, v[72:75], s[10:11]
	v_pk_mul_f32 v[224:225], v[200:201], v[72:73]
	v_pk_mul_f32 v[226:227], v[202:203], v[74:75]
	v_cvt_pk_bf16_f32 v228, v224, v225
	v_cvt_pk_bf16_f32 v229, v226, v227
	global_store_dwordx2 v62, v[228:229], s[28:29]
	v_pk_mul_f32 v[230:231], v[72:73], v[72:73]
	v_pk_mul_f32 v[232:233], v[74:75], v[74:75]
	v_add_f32_e32 v230, v230, v231
	v_add_f32_e32 v230, v232, v230
	v_add_f32_e32 v238, v233, v230
	v_pk_add_f32 v[88:89], v[88:89], v[40:41]
	v_pk_add_f32 v[90:91], v[90:91], v[42:43]
	global_store_dwordx4 v58, v[88:91], s[10:11] offset:64
	v_pk_mul_f32 v[224:225], v[204:205], v[88:89]
	v_pk_mul_f32 v[226:227], v[206:207], v[90:91]
	v_cvt_pk_bf16_f32 v228, v224, v225
	v_cvt_pk_bf16_f32 v229, v226, v227
	global_store_dwordx2 v62, v[228:229], s[28:29] offset:32
	v_pk_mul_f32 v[230:231], v[88:89], v[88:89]
	v_pk_mul_f32 v[232:233], v[90:91], v[90:91]
	v_add_f32_e32 v230, v230, v231
	v_add_f32_e32 v230, v232, v230
	v_add_f32_e32 v230, v233, v230
	v_add_f32_e32 v238, v238, v230
	v_pk_add_f32 v[104:105], v[104:105], v[240:241]
	v_pk_add_f32 v[106:107], v[106:107], v[242:243]
	global_store_dwordx4 v58, v[104:107], s[10:11] offset:128
	v_pk_mul_f32 v[224:225], v[208:209], v[104:105]
	v_pk_mul_f32 v[226:227], v[210:211], v[106:107]
	v_cvt_pk_bf16_f32 v228, v224, v225
	v_cvt_pk_bf16_f32 v229, v226, v227
	global_store_dwordx2 v62, v[228:229], s[28:29] offset:64
	v_pk_mul_f32 v[230:231], v[104:105], v[104:105]
	v_pk_mul_f32 v[232:233], v[106:107], v[106:107]
	v_add_f32_e32 v230, v230, v231
	v_add_f32_e32 v230, v232, v230
	v_add_f32_e32 v230, v233, v230
	v_add_f32_e32 v238, v238, v230
	v_pk_add_f32 v[120:121], v[120:121], v[160:161]
	v_pk_add_f32 v[122:123], v[122:123], v[162:163]
	global_store_dwordx4 v58, v[120:123], s[10:11] offset:192
	v_pk_mul_f32 v[224:225], v[212:213], v[120:121]
	v_pk_mul_f32 v[226:227], v[214:215], v[122:123]
	v_cvt_pk_bf16_f32 v228, v224, v225
	v_cvt_pk_bf16_f32 v229, v226, v227
	global_store_dwordx2 v62, v[228:229], s[28:29] offset:96
	v_pk_mul_f32 v[230:231], v[120:121], v[120:121]
	v_pk_mul_f32 v[232:233], v[122:123], v[122:123]
	v_add_f32_e32 v230, v230, v231
	v_add_f32_e32 v230, v232, v230
	v_add_f32_e32 v239, v233, v230
	v_pk_add_f32 v[136:137], v[136:137], v[176:177]
	v_pk_add_f32 v[138:139], v[138:139], v[178:179]
	global_store_dwordx4 v58, v[136:139], s[10:11] offset:256
	v_pk_mul_f32 v[224:225], v[216:217], v[136:137]
	v_pk_mul_f32 v[226:227], v[218:219], v[138:139]
	v_cvt_pk_bf16_f32 v228, v224, v225
	v_cvt_pk_bf16_f32 v229, v226, v227
	global_store_dwordx2 v62, v[228:229], s[28:29] offset:128
	v_pk_mul_f32 v[230:231], v[136:137], v[136:137]
	v_pk_mul_f32 v[232:233], v[138:139], v[138:139]
	v_add_f32_e32 v230, v230, v231
	v_add_f32_e32 v230, v232, v230
	v_add_f32_e32 v230, v233, v230
	v_add_f32_e32 v239, v239, v230
	v_pk_add_f32 v[152:153], v[152:153], v[192:193]
	v_pk_add_f32 v[154:155], v[154:155], v[194:195]
	global_store_dwordx4 v58, v[152:155], s[10:11] offset:320
	v_pk_mul_f32 v[224:225], v[220:221], v[152:153]
	v_pk_mul_f32 v[226:227], v[222:223], v[154:155]
	v_cvt_pk_bf16_f32 v228, v224, v225
	v_cvt_pk_bf16_f32 v229, v226, v227
	global_store_dwordx2 v62, v[228:229], s[28:29] offset:160
	v_pk_mul_f32 v[230:231], v[152:153], v[152:153]
	v_pk_mul_f32 v[232:233], v[154:155], v[154:155]
	v_add_f32_e32 v230, v230, v231
	v_add_f32_e32 v230, v232, v230
	v_add_f32_e32 v230, v233, v230
	v_add_f32_e32 v239, v239, v230
	v_pk_add_f32 v[76:77], v[76:77], v[28:29]
	v_pk_add_f32 v[78:79], v[78:79], v[30:31]
	global_store_dwordx4 v59, v[76:79], s[10:11]
	v_pk_mul_f32 v[224:225], v[200:201], v[76:77]
	v_pk_mul_f32 v[226:227], v[202:203], v[78:79]
	v_cvt_pk_bf16_f32 v228, v224, v225
	v_cvt_pk_bf16_f32 v229, v226, v227
	global_store_dwordx2 v63, v[228:229], s[28:29]
	v_pk_mul_f32 v[230:231], v[76:77], v[76:77]
	v_pk_mul_f32 v[232:233], v[78:79], v[78:79]
	v_add_f32_e32 v230, v230, v231
	v_add_f32_e32 v230, v232, v230
	v_add_f32_e32 v14, v233, v230
	v_pk_add_f32 v[92:93], v[92:93], v[44:45]
	v_pk_add_f32 v[94:95], v[94:95], v[46:47]
	global_store_dwordx4 v59, v[92:95], s[10:11] offset:64
	v_pk_mul_f32 v[224:225], v[204:205], v[92:93]
	v_pk_mul_f32 v[226:227], v[206:207], v[94:95]
	v_cvt_pk_bf16_f32 v228, v224, v225
	v_cvt_pk_bf16_f32 v229, v226, v227
	global_store_dwordx2 v63, v[228:229], s[28:29] offset:32
	v_pk_mul_f32 v[230:231], v[92:93], v[92:93]
	v_pk_mul_f32 v[232:233], v[94:95], v[94:95]
	v_add_f32_e32 v230, v230, v231
	v_add_f32_e32 v230, v232, v230
	v_add_f32_e32 v230, v233, v230
	v_add_f32_e32 v14, v14, v230
	v_pk_add_f32 v[108:109], v[108:109], v[244:245]
	v_pk_add_f32 v[110:111], v[110:111], v[246:247]
	global_store_dwordx4 v59, v[108:111], s[10:11] offset:128
	v_pk_mul_f32 v[224:225], v[208:209], v[108:109]
	v_pk_mul_f32 v[226:227], v[210:211], v[110:111]
	v_cvt_pk_bf16_f32 v228, v224, v225
	v_cvt_pk_bf16_f32 v229, v226, v227
	global_store_dwordx2 v63, v[228:229], s[28:29] offset:64
	v_pk_mul_f32 v[230:231], v[108:109], v[108:109]
	v_pk_mul_f32 v[232:233], v[110:111], v[110:111]
	v_add_f32_e32 v230, v230, v231
	v_add_f32_e32 v230, v232, v230
	v_add_f32_e32 v230, v233, v230
	v_add_f32_e32 v14, v14, v230
	v_pk_add_f32 v[124:125], v[124:125], v[164:165]
	v_pk_add_f32 v[126:127], v[126:127], v[166:167]
	global_store_dwordx4 v59, v[124:127], s[10:11] offset:192
	v_pk_mul_f32 v[224:225], v[212:213], v[124:125]
	v_pk_mul_f32 v[226:227], v[214:215], v[126:127]
	v_cvt_pk_bf16_f32 v228, v224, v225
	v_cvt_pk_bf16_f32 v229, v226, v227
	global_store_dwordx2 v63, v[228:229], s[28:29] offset:96
	v_pk_mul_f32 v[230:231], v[124:125], v[124:125]
	v_pk_mul_f32 v[232:233], v[126:127], v[126:127]
	v_add_f32_e32 v230, v230, v231
	v_add_f32_e32 v230, v232, v230
	v_add_f32_e32 v15, v233, v230
	v_pk_add_f32 v[140:141], v[140:141], v[180:181]
	v_pk_add_f32 v[142:143], v[142:143], v[182:183]
	global_store_dwordx4 v59, v[140:143], s[10:11] offset:256
	v_pk_mul_f32 v[224:225], v[216:217], v[140:141]
	v_pk_mul_f32 v[226:227], v[218:219], v[142:143]
	v_cvt_pk_bf16_f32 v228, v224, v225
	v_cvt_pk_bf16_f32 v229, v226, v227
	global_store_dwordx2 v63, v[228:229], s[28:29] offset:128
	v_pk_mul_f32 v[230:231], v[140:141], v[140:141]
	v_pk_mul_f32 v[232:233], v[142:143], v[142:143]
	v_add_f32_e32 v230, v230, v231
	v_add_f32_e32 v230, v232, v230
	v_add_f32_e32 v230, v233, v230
	v_add_f32_e32 v15, v15, v230
	v_pk_add_f32 v[156:157], v[156:157], v[196:197]
	v_pk_add_f32 v[158:159], v[158:159], v[198:199]
	global_store_dwordx4 v59, v[156:159], s[10:11] offset:320
	v_pk_mul_f32 v[224:225], v[220:221], v[156:157]
	v_pk_mul_f32 v[226:227], v[222:223], v[158:159]
	v_cvt_pk_bf16_f32 v228, v224, v225
	v_cvt_pk_bf16_f32 v229, v226, v227
	global_store_dwordx2 v63, v[228:229], s[28:29] offset:160
	v_pk_mul_f32 v[230:231], v[156:157], v[156:157]
	v_pk_mul_f32 v[232:233], v[158:159], v[158:159]
	v_add_f32_e32 v230, v230, v231
	v_add_f32_e32 v230, v232, v230
	v_add_f32_e32 v230, v233, v230
	v_add_f32_e32 v15, v15, v230
	ds_bpermute_b32 v224, v13, v234
	ds_bpermute_b32 v225, v13, v235
	ds_bpermute_b32 v226, v13, v236
	ds_bpermute_b32 v227, v13, v237
	ds_bpermute_b32 v228, v13, v238
	ds_bpermute_b32 v229, v13, v239
	ds_bpermute_b32 v230, v13, v14
	ds_bpermute_b32 v231, v13, v15
	s_waitcnt lgkmcnt(0)
	v_add_f32_e32 v234, v234, v224
	v_add_f32_e32 v235, v235, v225
	v_add_f32_e32 v236, v236, v226
	v_add_f32_e32 v237, v237, v227
	v_add_f32_e32 v238, v238, v228
	v_add_f32_e32 v239, v239, v229
	v_add_f32_e32 v14, v14, v230
	v_add_f32_e32 v15, v15, v231
	ds_bpermute_b32 v224, v12, v234
	ds_bpermute_b32 v225, v12, v235
	ds_bpermute_b32 v226, v12, v236
	ds_bpermute_b32 v227, v12, v237
	ds_bpermute_b32 v228, v12, v238
	ds_bpermute_b32 v229, v12, v239
	ds_bpermute_b32 v230, v12, v14
	ds_bpermute_b32 v231, v12, v15
	s_waitcnt lgkmcnt(0)
	v_add_f32_e32 v234, v234, v224
	v_add_f32_e32 v235, v235, v225
	v_add_f32_e32 v236, v236, v226
	v_add_f32_e32 v237, v237, v227
	v_add_f32_e32 v238, v238, v228
	v_add_f32_e32 v239, v239, v229
	v_add_f32_e32 v14, v14, v230
	v_add_f32_e32 v15, v15, v231
	s_and_saveexec_b64 s[2:3], vcc
	global_store_dwordx2 v8, v[234:235], s[26:27]
	global_store_dwordx2 v9, v[236:237], s[26:27]
	global_store_dwordx2 v10, v[238:239], s[26:27]
	global_store_dwordx2 v11, v[14:15], s[26:27]
	s_or_b64 exec, exec, s[2:3]

.Ldn_loop:
	s_waitcnt lgkmcnt(0)
	v_mfma_f32_16x16x32_bf16 v[64:67], v[176:179], v[160:163], v[64:67]
	ds_read_b128 v[200:203], v11 offset:0
	v_mfma_f32_16x16x32_bf16 v[68:71], v[176:179], v[164:167], v[68:71]
	s_add_u32 m0, s20, 0x5000
	v_mfma_f32_16x16x32_bf16 v[72:75], v[176:179], v[168:171], v[72:75]
	ds_read_b128 v[204:207], v11 offset:2048
	v_mfma_f32_16x16x32_bf16 v[76:79], v[176:179], v[172:175], v[76:79]
	global_load_lds_dwordx4 v3, s[18:19]
	v_mfma_f32_16x16x32_bf16 v[80:83], v[180:183], v[160:163], v[80:83]
	ds_read_b128 v[208:211], v11 offset:4096
	v_mfma_f32_16x16x32_bf16 v[84:87], v[180:183], v[164:167], v[84:87]
	s_add_u32 m0, s20, 0x6000
	v_mfma_f32_16x16x32_bf16 v[88:91], v[180:183], v[168:171], v[88:91]
	ds_read_b128 v[212:215], v11 offset:6144
	v_mfma_f32_16x16x32_bf16 v[92:95], v[180:183], v[172:175], v[92:95]
	global_load_lds_dwordx4 v4, s[18:19]
	v_mfma_f32_16x16x32_bf16 v[96:99], v[184:187], v[160:163], v[96:99]
	ds_read_b128 v[216:219], v13 offset:0
	v_mfma_f32_16x16x32_bf16 v[100:103], v[184:187], v[164:167], v[100:103]
	s_add_u32 m0, s20, 0x7000
	v_mfma_f32_16x16x32_bf16 v[104:107], v[184:187], v[168:171], v[104:107]
	ds_read_b128 v[220:223], v13 offset:2048
	v_mfma_f32_16x16x32_bf16 v[108:111], v[184:187], v[172:175], v[108:111]
	global_load_lds_dwordx4 v5, s[18:19]
	v_mfma_f32_16x16x32_bf16 v[112:115], v[188:191], v[160:163], v[112:115]
	ds_read_b128 v[224:227], v13 offset:4096
	v_mfma_f32_16x16x32_bf16 v[116:119], v[188:191], v[164:167], v[116:119]
	s_add_u32 m0, s20, 0x8000
	v_mfma_f32_16x16x32_bf16 v[120:123], v[188:191], v[168:171], v[120:123]
	ds_read_b128 v[228:231], v13 offset:6144
	v_mfma_f32_16x16x32_bf16 v[124:127], v[188:191], v[172:175], v[124:127]
	global_load_lds_dwordx4 v6, s[18:19]
	v_mfma_f32_16x16x32_bf16 v[128:131], v[192:195], v[160:163], v[128:131]
	ds_read_b128 v[232:235], v13 offset:8192
	v_mfma_f32_16x16x32_bf16 v[132:135], v[192:195], v[164:167], v[132:135]
	s_add_u32 m0, s20, 0x9000
	v_mfma_f32_16x16x32_bf16 v[136:139], v[192:195], v[168:171], v[136:139]
	ds_read_b128 v[236:239], v13 offset:10240
	v_mfma_f32_16x16x32_bf16 v[140:143], v[192:195], v[172:175], v[140:143]
	global_load_lds_dwordx4 v7, s[18:19]
	v_mfma_f32_16x16x32_bf16 v[144:147], v[196:199], v[160:163], v[144:147]
	s_add_u32 s16, s16, 0x80
	s_addc_u32 s17, s17, 0
	s_add_u32 s18, s18, 0x80
	s_addc_u32 s19, s19, 0
	v_mfma_f32_16x16x32_bf16 v[148:151], v[196:199], v[164:167], v[148:151]
	s_add_u32 s20, s20, 0xa000
	s_sub_u32 s22, s20, 0x28000
	s_cmp_ge_u32 s20, 0x28000
	s_cselect_b32 s20, s22, s20
	v_mfma_f32_16x16x32_bf16 v[152:155], v[196:199], v[168:171], v[152:155]
	v_add_u32_e32 v10, s21, v8
	v_add_u32_e32 v12, s21, v9
	v_xor_b32_e32 v11, 64, v10
	v_xor_b32_e32 v13, 64, v12
	v_mfma_f32_16x16x32_bf16 v[156:159], v[196:199], v[172:175], v[156:159]
	s_add_u32 s21, s21, 0xa000
	s_sub_u32 s23, s21, 0x28000
	s_cmp_ge_u32 s21, 0x28000
	s_cselect_b32 s21, s23, s21
	s_waitcnt lgkmcnt(0)
	v_mfma_f32_16x16x32_bf16 v[64:67], v[216:219], v[200:203], v[64:67]
	v_mfma_f32_16x16x32_bf16 v[68:71], v[216:219], v[204:207], v[68:71]
	v_mfma_f32_16x16x32_bf16 v[72:75], v[216:219], v[208:211], v[72:75]
	v_mfma_f32_16x16x32_bf16 v[76:79], v[216:219], v[212:215], v[76:79]
	s_waitcnt vmcnt(20)
	s_barrier
	v_mfma_f32_16x16x32_bf16 v[80:83], v[220:223], v[200:203], v[80:83]
	ds_read_b128 v[160:163], v10 offset:0
	v_mfma_f32_16x16x32_bf16 v[84:87], v[220:223], v[204:207], v[84:87]
	s_add_u32 m0, s20, 0x0
	v_mfma_f32_16x16x32_bf16 v[88:91], v[220:223], v[208:211], v[88:91]
	ds_read_b128 v[164:167], v10 offset:2048
	v_mfma_f32_16x16x32_bf16 v[92:95], v[220:223], v[212:215], v[92:95]
	global_load_lds_dwordx4 v2, s[16:17]
	v_mfma_f32_16x16x32_bf16 v[96:99], v[224:227], v[200:203], v[96:99]
	ds_read_b128 v[168:171], v10 offset:4096
	v_mfma_f32_16x16x32_bf16 v[100:103], v[224:227], v[204:207], v[100:103]
	s_add_u32 m0, s20, 0x1000
	v_mfma_f32_16x16x32_bf16 v[104:107], v[224:227], v[208:211], v[104:107]
	ds_read_b128 v[172:175], v10 offset:6144
	v_mfma_f32_16x16x32_bf16 v[108:111], v[224:227], v[212:215], v[108:111]
	global_load_lds_dwordx4 v3, s[16:17]
	v_mfma_f32_16x16x32_bf16 v[112:115], v[228:231], v[200:203], v[112:115]
	ds_read_b128 v[176:179], v12 offset:0
	v_mfma_f32_16x16x32_bf16 v[116:119], v[228:231], v[204:207], v[116:119]
	s_add_u32 m0, s20, 0x2000
	v_mfma_f32_16x16x32_bf16 v[120:123], v[228:231], v[208:211], v[120:123]
	ds_read_b128 v[180:183], v12 offset:2048
	v_mfma_f32_16x16x32_bf16 v[124:127], v[228:231], v[212:215], v[124:127]
	global_load_lds_dwordx4 v4, s[16:17]
	v_mfma_f32_16x16x32_bf16 v[128:131], v[232:235], v[200:203], v[128:131]
	ds_read_b128 v[184:187], v12 offset:4096
	v_mfma_f32_16x16x32_bf16 v[132:135], v[232:235], v[204:207], v[132:135]
	s_add_u32 m0, s20, 0x3000
	v_mfma_f32_16x16x32_bf16 v[136:139], v[232:235], v[208:211], v[136:139]
	ds_read_b128 v[188:191], v12 offset:6144
	v_mfma_f32_16x16x32_bf16 v[140:143], v[232:235], v[212:215], v[140:143]
	global_load_lds_dwordx4 v5, s[16:17]
	v_mfma_f32_16x16x32_bf16 v[144:147], v[236:239], v[200:203], v[144:147]
	ds_read_b128 v[192:195], v12 offset:8192
	v_mfma_f32_16x16x32_bf16 v[148:151], v[236:239], v[204:207], v[148:151]
	s_add_u32 m0, s20, 0x4000
	v_mfma_f32_16x16x32_bf16 v[152:155], v[236:239], v[208:211], v[152:155]
	ds_read_b128 v[196:199], v12 offset:10240
	v_mfma_f32_16x16x32_bf16 v[156:159], v[236:239], v[212:215], v[156:159]
	global_load_lds_dwordx4 v2, s[18:19]
	s_add_u32 s15, s15, 1
	s_cmp_lt_u32 s15, 44
	s_cbranch_scc1 .Ldn_loop
	s_waitcnt lgkmcnt(0)
	v_mfma_f32_16x16x32_bf16 v[64:67], v[176:179], v[160:163], v[64:67]
	ds_read_b128 v[200:203], v11 offset:0
	v_mfma_f32_16x16x32_bf16 v[68:71], v[176:179], v[164:167], v[68:71]
	s_add_u32 m0, s20, 0x5000
	v_mfma_f32_16x16x32_bf16 v[72:75], v[176:179], v[168:171], v[72:75]
	ds_read_b128 v[204:207], v11 offset:2048
	v_mfma_f32_16x16x32_bf16 v[76:79], v[176:179], v[172:175], v[76:79]
	global_load_lds_dwordx4 v3, s[18:19]
	v_mfma_f32_16x16x32_bf16 v[80:83], v[180:183], v[160:163], v[80:83]
	ds_read_b128 v[208:211], v11 offset:4096
	v_mfma_f32_16x16x32_bf16 v[84:87], v[180:183], v[164:167], v[84:87]
	s_add_u32 m0, s20, 0x6000
	v_mfma_f32_16x16x32_bf16 v[88:91], v[180:183], v[168:171], v[88:91]
	ds_read_b128 v[212:215], v11 offset:6144
	v_mfma_f32_16x16x32_bf16 v[92:95], v[180:183], v[172:175], v[92:95]
	global_load_lds_dwordx4 v4, s[18:19]
	v_mfma_f32_16x16x32_bf16 v[96:99], v[184:187], v[160:163], v[96:99]
	ds_read_b128 v[216:219], v13 offset:0
	v_mfma_f32_16x16x32_bf16 v[100:103], v[184:187], v[164:167], v[100:103]
	s_add_u32 m0, s20, 0x7000
	v_mfma_f32_16x16x32_bf16 v[104:107], v[184:187], v[168:171], v[104:107]
	ds_read_b128 v[220:223], v13 offset:2048
	v_mfma_f32_16x16x32_bf16 v[108:111], v[184:187], v[172:175], v[108:111]
	global_load_lds_dwordx4 v5, s[18:19]
	v_mfma_f32_16x16x32_bf16 v[112:115], v[188:191], v[160:163], v[112:115]
	ds_read_b128 v[224:227], v13 offset:4096
	v_mfma_f32_16x16x32_bf16 v[116:119], v[188:191], v[164:167], v[116:119]
	s_add_u32 m0, s20, 0x8000
	v_mfma_f32_16x16x32_bf16 v[120:123], v[188:191], v[168:171], v[120:123]
	ds_read_b128 v[228:231], v13 offset:6144
	v_mfma_f32_16x16x32_bf16 v[124:127], v[188:191], v[172:175], v[124:127]
	global_load_lds_dwordx4 v6, s[18:19]
	v_mfma_f32_16x16x32_bf16 v[128:131], v[192:195], v[160:163], v[128:131]
	ds_read_b128 v[232:235], v13 offset:8192
	v_mfma_f32_16x16x32_bf16 v[132:135], v[192:195], v[164:167], v[132:135]
	s_add_u32 m0, s20, 0x9000
	v_mfma_f32_16x16x32_bf16 v[136:139], v[192:195], v[168:171], v[136:139]
	ds_read_b128 v[236:239], v13 offset:10240
	v_mfma_f32_16x16x32_bf16 v[140:143], v[192:195], v[172:175], v[140:143]
	global_load_lds_dwordx4 v7, s[18:19]
	v_mfma_f32_16x16x32_bf16 v[144:147], v[196:199], v[160:163], v[144:147]
	s_add_u32 s16, s16, 0x80
	s_addc_u32 s17, s17, 0
	s_add_u32 s18, s18, 0x80
	s_addc_u32 s19, s19, 0
	v_mfma_f32_16x16x32_bf16 v[148:151], v[196:199], v[164:167], v[148:151]
	s_add_u32 s20, s20, 0xa000
	s_sub_u32 s22, s20, 0x28000
	s_cmp_ge_u32 s20, 0x28000
	s_cselect_b32 s20, s22, s20
	v_mfma_f32_16x16x32_bf16 v[152:155], v[196:199], v[168:171], v[152:155]
	v_add_u32_e32 v10, s21, v8
	v_add_u32_e32 v12, s21, v9
	v_xor_b32_e32 v11, 64, v10
	v_xor_b32_e32 v13, 64, v12
	v_mfma_f32_16x16x32_bf16 v[156:159], v[196:199], v[172:175], v[156:159]
	s_add_u32 s21, s21, 0xa000
	s_sub_u32 s23, s21, 0x28000
	s_cmp_ge_u32 s21, 0x28000
	s_cselect_b32 s21, s23, s21
	s_waitcnt lgkmcnt(0)
	v_mfma_f32_16x16x32_bf16 v[64:67], v[216:219], v[200:203], v[64:67]
	v_mfma_f32_16x16x32_bf16 v[68:71], v[216:219], v[204:207], v[68:71]
	v_mfma_f32_16x16x32_bf16 v[72:75], v[216:219], v[208:211], v[72:75]
	v_mfma_f32_16x16x32_bf16 v[76:79], v[216:219], v[212:215], v[76:79]
	s_waitcnt vmcnt(20)
	s_barrier
	v_mfma_f32_16x16x32_bf16 v[80:83], v[220:223], v[200:203], v[80:83]
	ds_read_b128 v[160:163], v10 offset:0
	v_mfma_f32_16x16x32_bf16 v[84:87], v[220:223], v[204:207], v[84:87]
	global_load_dwordx4 v[16:19], v56, s[8:9] offset:0
	v_mfma_f32_16x16x32_bf16 v[88:91], v[220:223], v[208:211], v[88:91]
	ds_read_b128 v[164:167], v10 offset:2048
	v_mfma_f32_16x16x32_bf16 v[92:95], v[220:223], v[212:215], v[92:95]
	global_load_dwordx4 v[20:23], v57, s[8:9] offset:0
	v_mfma_f32_16x16x32_bf16 v[96:99], v[224:227], v[200:203], v[96:99]
	ds_read_b128 v[168:171], v10 offset:4096
	v_mfma_f32_16x16x32_bf16 v[100:103], v[224:227], v[204:207], v[100:103]
	global_load_dwordx4 v[24:27], v58, s[8:9] offset:0
	v_mfma_f32_16x16x32_bf16 v[104:107], v[224:227], v[208:211], v[104:107]
	ds_read_b128 v[172:175], v10 offset:6144
	v_mfma_f32_16x16x32_bf16 v[108:111], v[224:227], v[212:215], v[108:111]
	global_load_dwordx4 v[28:31], v59, s[8:9] offset:0
	v_mfma_f32_16x16x32_bf16 v[112:115], v[228:231], v[200:203], v[112:115]
	ds_read_b128 v[176:179], v12 offset:0
	v_mfma_f32_16x16x32_bf16 v[116:119], v[228:231], v[204:207], v[116:119]
	global_load_dwordx4 v[32:35], v56, s[8:9] offset:64
	v_mfma_f32_16x16x32_bf16 v[120:123], v[228:231], v[208:211], v[120:123]
	ds_read_b128 v[180:183], v12 offset:2048
	v_mfma_f32_16x16x32_bf16 v[124:127], v[228:231], v[212:215], v[124:127]
	global_load_dwordx4 v[36:39], v57, s[8:9] offset:64
	v_mfma_f32_16x16x32_bf16 v[128:131], v[232:235], v[200:203], v[128:131]
	ds_read_b128 v[184:187], v12 offset:4096
	v_mfma_f32_16x16x32_bf16 v[132:135], v[232:235], v[204:207], v[132:135]
	global_load_dwordx4 v[40:43], v58, s[8:9] offset:64
	v_mfma_f32_16x16x32_bf16 v[136:139], v[232:235], v[208:211], v[136:139]
	ds_read_b128 v[188:191], v12 offset:6144
	v_mfma_f32_16x16x32_bf16 v[140:143], v[232:235], v[212:215], v[140:143]
	global_load_dwordx4 v[44:47], v59, s[8:9] offset:64
	v_mfma_f32_16x16x32_bf16 v[144:147], v[236:239], v[200:203], v[144:147]
	ds_read_b128 v[192:195], v12 offset:8192
	v_mfma_f32_16x16x32_bf16 v[148:151], v[236:239], v[204:207], v[148:151]
	global_load_dwordx4 v[48:51], v56, s[8:9] offset:128
	v_mfma_f32_16x16x32_bf16 v[152:155], v[236:239], v[208:211], v[152:155]
	ds_read_b128 v[196:199], v12 offset:10240
	v_mfma_f32_16x16x32_bf16 v[156:159], v[236:239], v[212:215], v[156:159]
	global_load_dwordx4 v[52:55], v57, s[8:9] offset:128
	global_load_dwordx4 v[240:243], v58, s[8:9] offset:128
	global_load_dwordx4 v[244:247], v59, s[8:9] offset:128
	global_load_dwordx4 v[248:251], v56, s[8:9] offset:192
	global_load_dwordx4 v[252:255], v57, s[8:9] offset:192
	s_waitcnt lgkmcnt(0)
	v_mfma_f32_16x16x32_bf16 v[64:67], v[176:179], v[160:163], v[64:67]
	ds_read_b128 v[200:203], v11 offset:0
	v_mfma_f32_16x16x32_bf16 v[68:71], v[176:179], v[164:167], v[68:71]
	ds_read_b128 v[204:207], v11 offset:2048
	v_mfma_f32_16x16x32_bf16 v[72:75], v[176:179], v[168:171], v[72:75]
	ds_read_b128 v[208:211], v11 offset:4096
	v_mfma_f32_16x16x32_bf16 v[76:79], v[176:179], v[172:175], v[76:79]
	ds_read_b128 v[212:215], v11 offset:6144
	v_mfma_f32_16x16x32_bf16 v[80:83], v[180:183], v[160:163], v[80:83]
	ds_read_b128 v[216:219], v13 offset:0
	v_mfma_f32_16x16x32_bf16 v[84:87], v[180:183], v[164:167], v[84:87]
	ds_read_b128 v[220:223], v13 offset:2048
	v_mfma_f32_16x16x32_bf16 v[88:91], v[180:183], v[168:171], v[88:91]
	ds_read_b128 v[224:227], v13 offset:4096
	v_mfma_f32_16x16x32_bf16 v[92:95], v[180:183], v[172:175], v[92:95]
	ds_read_b128 v[228:231], v13 offset:6144
	v_mfma_f32_16x16x32_bf16 v[96:99], v[184:187], v[160:163], v[96:99]
	ds_read_b128 v[232:235], v13 offset:8192
	v_mfma_f32_16x16x32_bf16 v[100:103], v[184:187], v[164:167], v[100:103]
	ds_read_b128 v[236:239], v13 offset:10240
	v_mfma_f32_16x16x32_bf16 v[104:107], v[184:187], v[168:171], v[104:107]
	v_mfma_f32_16x16x32_bf16 v[108:111], v[184:187], v[172:175], v[108:111]
	v_mfma_f32_16x16x32_bf16 v[112:115], v[188:191], v[160:163], v[112:115]
	v_mfma_f32_16x16x32_bf16 v[116:119], v[188:191], v[164:167], v[116:119]
	v_mfma_f32_16x16x32_bf16 v[120:123], v[188:191], v[168:171], v[120:123]
	v_mfma_f32_16x16x32_bf16 v[124:127], v[188:191], v[172:175], v[124:127]
	v_mfma_f32_16x16x32_bf16 v[128:131], v[192:195], v[160:163], v[128:131]
	v_mfma_f32_16x16x32_bf16 v[132:135], v[192:195], v[164:167], v[132:135]
	v_mfma_f32_16x16x32_bf16 v[136:139], v[192:195], v[168:171], v[136:139]
	v_mfma_f32_16x16x32_bf16 v[140:143], v[192:195], v[172:175], v[140:143]
	v_mfma_f32_16x16x32_bf16 v[144:147], v[196:199], v[160:163], v[144:147]
	v_add_u32_e32 v10, s21, v8
	v_add_u32_e32 v12, s21, v9
	v_xor_b32_e32 v11, 64, v10
	v_xor_b32_e32 v13, 64, v12
	v_mfma_f32_16x16x32_bf16 v[148:151], v[196:199], v[164:167], v[148:151]
	s_add_u32 s21, s21, 0xa000
	s_sub_u32 s23, s21, 0x28000
	s_cmp_ge_u32 s21, 0x28000
	s_cselect_b32 s21, s23, s21
	v_mfma_f32_16x16x32_bf16 v[152:155], v[196:199], v[168:171], v[152:155]
	v_mfma_f32_16x16x32_bf16 v[156:159], v[196:199], v[172:175], v[156:159]
	s_waitcnt lgkmcnt(0)
	v_mfma_f32_16x16x32_bf16 v[64:67], v[216:219], v[200:203], v[64:67]
	v_mfma_f32_16x16x32_bf16 v[68:71], v[216:219], v[204:207], v[68:71]
	v_mfma_f32_16x16x32_bf16 v[72:75], v[216:219], v[208:211], v[72:75]
	v_mfma_f32_16x16x32_bf16 v[76:79], v[216:219], v[212:215], v[76:79]
	s_waitcnt vmcnt(24)
	s_barrier
	v_mfma_f32_16x16x32_bf16 v[80:83], v[220:223], v[200:203], v[80:83]
	ds_read_b128 v[160:163], v10 offset:0
	v_mfma_f32_16x16x32_bf16 v[84:87], v[220:223], v[204:207], v[84:87]
	ds_read_b128 v[164:167], v10 offset:2048
	v_mfma_f32_16x16x32_bf16 v[88:91], v[220:223], v[208:211], v[88:91]
	ds_read_b128 v[168:171], v10 offset:4096
	v_mfma_f32_16x16x32_bf16 v[92:95], v[220:223], v[212:215], v[92:95]
	ds_read_b128 v[172:175], v10 offset:6144
	v_mfma_f32_16x16x32_bf16 v[96:99], v[224:227], v[200:203], v[96:99]
	ds_read_b128 v[176:179], v12 offset:0
	v_mfma_f32_16x16x32_bf16 v[100:103], v[224:227], v[204:207], v[100:103]
	ds_read_b128 v[180:183], v12 offset:2048
	v_mfma_f32_16x16x32_bf16 v[104:107], v[224:227], v[208:211], v[104:107]
	ds_read_b128 v[184:187], v12 offset:4096
	v_mfma_f32_16x16x32_bf16 v[108:111], v[224:227], v[212:215], v[108:111]
	ds_read_b128 v[188:191], v12 offset:6144
	v_mfma_f32_16x16x32_bf16 v[112:115], v[228:231], v[200:203], v[112:115]
	ds_read_b128 v[192:195], v12 offset:8192
	v_mfma_f32_16x16x32_bf16 v[116:119], v[228:231], v[204:207], v[116:119]
	ds_read_b128 v[196:199], v12 offset:10240
	v_mfma_f32_16x16x32_bf16 v[120:123], v[228:231], v[208:211], v[120:123]
	v_mfma_f32_16x16x32_bf16 v[124:127], v[228:231], v[212:215], v[124:127]
	v_mfma_f32_16x16x32_bf16 v[128:131], v[232:235], v[200:203], v[128:131]
	v_mfma_f32_16x16x32_bf16 v[132:135], v[232:235], v[204:207], v[132:135]
	v_mfma_f32_16x16x32_bf16 v[136:139], v[232:235], v[208:211], v[136:139]
	v_mfma_f32_16x16x32_bf16 v[140:143], v[232:235], v[212:215], v[140:143]
	v_mfma_f32_16x16x32_bf16 v[144:147], v[236:239], v[200:203], v[144:147]
	v_mfma_f32_16x16x32_bf16 v[148:151], v[236:239], v[204:207], v[148:151]
	v_mfma_f32_16x16x32_bf16 v[152:155], v[236:239], v[208:211], v[152:155]
	v_mfma_f32_16x16x32_bf16 v[156:159], v[236:239], v[212:215], v[156:159]
	s_waitcnt lgkmcnt(0)
	v_mfma_f32_16x16x32_bf16 v[64:67], v[176:179], v[160:163], v[64:67]
	ds_read_b128 v[200:203], v11 offset:0
	v_mfma_f32_16x16x32_bf16 v[68:71], v[176:179], v[164:167], v[68:71]
	ds_read_b128 v[204:207], v11 offset:2048
	v_mfma_f32_16x16x32_bf16 v[72:75], v[176:179], v[168:171], v[72:75]
	ds_read_b128 v[208:211], v11 offset:4096
	v_mfma_f32_16x16x32_bf16 v[76:79], v[176:179], v[172:175], v[76:79]
	ds_read_b128 v[212:215], v11 offset:6144
	v_mfma_f32_16x16x32_bf16 v[80:83], v[180:183], v[160:163], v[80:83]
	ds_read_b128 v[216:219], v13 offset:0
	v_mfma_f32_16x16x32_bf16 v[84:87], v[180:183], v[164:167], v[84:87]
	ds_read_b128 v[220:223], v13 offset:2048
	v_mfma_f32_16x16x32_bf16 v[88:91], v[180:183], v[168:171], v[88:91]
	ds_read_b128 v[224:227], v13 offset:4096
	v_mfma_f32_16x16x32_bf16 v[92:95], v[180:183], v[172:175], v[92:95]
	ds_read_b128 v[228:231], v13 offset:6144
	v_mfma_f32_16x16x32_bf16 v[96:99], v[184:187], v[160:163], v[96:99]
	ds_read_b128 v[232:235], v13 offset:8192
	v_mfma_f32_16x16x32_bf16 v[100:103], v[184:187], v[164:167], v[100:103]
	ds_read_b128 v[236:239], v13 offset:10240
	v_mfma_f32_16x16x32_bf16 v[104:107], v[184:187], v[168:171], v[104:107]
	v_mfma_f32_16x16x32_bf16 v[108:111], v[184:187], v[172:175], v[108:111]
	v_mfma_f32_16x16x32_bf16 v[112:115], v[188:191], v[160:163], v[112:115]
	v_mfma_f32_16x16x32_bf16 v[116:119], v[188:191], v[164:167], v[116:119]
	v_mfma_f32_16x16x32_bf16 v[120:123], v[188:191], v[168:171], v[120:123]
	v_mfma_f32_16x16x32_bf16 v[124:127], v[188:191], v[172:175], v[124:127]
	v_mfma_f32_16x16x32_bf16 v[128:131], v[192:195], v[160:163], v[128:131]
	v_mfma_f32_16x16x32_bf16 v[132:135], v[192:195], v[164:167], v[132:135]
	v_mfma_f32_16x16x32_bf16 v[136:139], v[192:195], v[168:171], v[136:139]
	v_mfma_f32_16x16x32_bf16 v[140:143], v[192:195], v[172:175], v[140:143]
	v_mfma_f32_16x16x32_bf16 v[144:147], v[196:199], v[160:163], v[144:147]
	v_add_u32_e32 v10, s21, v8
	v_add_u32_e32 v12, s21, v9
	v_xor_b32_e32 v11, 64, v10
	v_xor_b32_e32 v13, 64, v12
	v_mfma_f32_16x16x32_bf16 v[148:151], v[196:199], v[164:167], v[148:151]
	s_add_u32 s21, s21, 0xa000
	s_sub_u32 s23, s21, 0x28000
	s_cmp_ge_u32 s21, 0x28000
	s_cselect_b32 s21, s23, s21
	v_mfma_f32_16x16x32_bf16 v[152:155], v[196:199], v[168:171], v[152:155]
	v_mfma_f32_16x16x32_bf16 v[156:159], v[196:199], v[172:175], v[156:159]
	s_waitcnt lgkmcnt(0)
	v_mfma_f32_16x16x32_bf16 v[64:67], v[216:219], v[200:203], v[64:67]
	v_mfma_f32_16x16x32_bf16 v[68:71], v[216:219], v[204:207], v[68:71]
	v_mfma_f32_16x16x32_bf16 v[72:75], v[216:219], v[208:211], v[72:75]
	v_mfma_f32_16x16x32_bf16 v[76:79], v[216:219], v[212:215], v[76:79]
	s_waitcnt vmcnt(14)
	s_barrier
	v_mfma_f32_16x16x32_bf16 v[80:83], v[220:223], v[200:203], v[80:83]
	ds_read_b128 v[160:163], v10 offset:0
	v_mfma_f32_16x16x32_bf16 v[84:87], v[220:223], v[204:207], v[84:87]
	ds_read_b128 v[164:167], v10 offset:2048
	v_mfma_f32_16x16x32_bf16 v[88:91], v[220:223], v[208:211], v[88:91]
	ds_read_b128 v[168:171], v10 offset:4096
	v_mfma_f32_16x16x32_bf16 v[92:95], v[220:223], v[212:215], v[92:95]
	ds_read_b128 v[172:175], v10 offset:6144
	v_mfma_f32_16x16x32_bf16 v[96:99], v[224:227], v[200:203], v[96:99]
	ds_read_b128 v[176:179], v12 offset:0
	v_mfma_f32_16x16x32_bf16 v[100:103], v[224:227], v[204:207], v[100:103]
	ds_read_b128 v[180:183], v12 offset:2048
	v_mfma_f32_16x16x32_bf16 v[104:107], v[224:227], v[208:211], v[104:107]
	ds_read_b128 v[184:187], v12 offset:4096
	v_mfma_f32_16x16x32_bf16 v[108:111], v[224:227], v[212:215], v[108:111]
	ds_read_b128 v[188:191], v12 offset:6144
	v_mfma_f32_16x16x32_bf16 v[112:115], v[228:231], v[200:203], v[112:115]
	ds_read_b128 v[192:195], v12 offset:8192
	v_mfma_f32_16x16x32_bf16 v[116:119], v[228:231], v[204:207], v[116:119]
	ds_read_b128 v[196:199], v12 offset:10240
	v_mfma_f32_16x16x32_bf16 v[120:123], v[228:231], v[208:211], v[120:123]
	v_mfma_f32_16x16x32_bf16 v[124:127], v[228:231], v[212:215], v[124:127]
	v_mfma_f32_16x16x32_bf16 v[128:131], v[232:235], v[200:203], v[128:131]
	v_mfma_f32_16x16x32_bf16 v[132:135], v[232:235], v[204:207], v[132:135]
	v_mfma_f32_16x16x32_bf16 v[136:139], v[232:235], v[208:211], v[136:139]
	v_mfma_f32_16x16x32_bf16 v[140:143], v[232:235], v[212:215], v[140:143]
	v_mfma_f32_16x16x32_bf16 v[144:147], v[236:239], v[200:203], v[144:147]
	v_mfma_f32_16x16x32_bf16 v[148:151], v[236:239], v[204:207], v[148:151]
	v_mfma_f32_16x16x32_bf16 v[152:155], v[236:239], v[208:211], v[152:155]
	v_mfma_f32_16x16x32_bf16 v[156:159], v[236:239], v[212:215], v[156:159]
	s_waitcnt lgkmcnt(0)
	v_mfma_f32_16x16x32_bf16 v[64:67], v[176:179], v[160:163], v[64:67]
	ds_read_b128 v[200:203], v11 offset:0
	v_mfma_f32_16x16x32_bf16 v[68:71], v[176:179], v[164:167], v[68:71]
	ds_read_b128 v[204:207], v11 offset:2048
	v_mfma_f32_16x16x32_bf16 v[72:75], v[176:179], v[168:171], v[72:75]
	ds_read_b128 v[208:211], v11 offset:4096
	v_mfma_f32_16x16x32_bf16 v[76:79], v[176:179], v[172:175], v[76:79]
	ds_read_b128 v[212:215], v11 offset:6144
	v_mfma_f32_16x16x32_bf16 v[80:83], v[180:183], v[160:163], v[80:83]
	ds_read_b128 v[216:219], v13 offset:0
	v_mfma_f32_16x16x32_bf16 v[84:87], v[180:183], v[164:167], v[84:87]
	ds_read_b128 v[220:223], v13 offset:2048
	v_mfma_f32_16x16x32_bf16 v[88:91], v[180:183], v[168:171], v[88:91]
	ds_read_b128 v[224:227], v13 offset:4096
	v_mfma_f32_16x16x32_bf16 v[92:95], v[180:183], v[172:175], v[92:95]
	ds_read_b128 v[228:231], v13 offset:6144
	v_mfma_f32_16x16x32_bf16 v[96:99], v[184:187], v[160:163], v[96:99]
	ds_read_b128 v[232:235], v13 offset:8192
	v_mfma_f32_16x16x32_bf16 v[100:103], v[184:187], v[164:167], v[100:103]
	ds_read_b128 v[236:239], v13 offset:10240
	v_mfma_f32_16x16x32_bf16 v[104:107], v[184:187], v[168:171], v[104:107]
	v_mfma_f32_16x16x32_bf16 v[108:111], v[184:187], v[172:175], v[108:111]
	v_mfma_f32_16x16x32_bf16 v[112:115], v[188:191], v[160:163], v[112:115]
	v_mfma_f32_16x16x32_bf16 v[116:119], v[188:191], v[164:167], v[116:119]
	v_mfma_f32_16x16x32_bf16 v[120:123], v[188:191], v[168:171], v[120:123]
	v_mfma_f32_16x16x32_bf16 v[124:127], v[188:191], v[172:175], v[124:127]
	v_mfma_f32_16x16x32_bf16 v[128:131], v[192:195], v[160:163], v[128:131]
	v_mfma_f32_16x16x32_bf16 v[132:135], v[192:195], v[164:167], v[132:135]
	v_mfma_f32_16x16x32_bf16 v[136:139], v[192:195], v[168:171], v[136:139]
	v_mfma_f32_16x16x32_bf16 v[140:143], v[192:195], v[172:175], v[140:143]
	v_mfma_f32_16x16x32_bf16 v[144:147], v[196:199], v[160:163], v[144:147]
	v_mfma_f32_16x16x32_bf16 v[148:151], v[196:199], v[164:167], v[148:151]
	v_mfma_f32_16x16x32_bf16 v[152:155], v[196:199], v[168:171], v[152:155]
	v_mfma_f32_16x16x32_bf16 v[156:159], v[196:199], v[172:175], v[156:159]
	s_waitcnt lgkmcnt(0)
	v_mfma_f32_16x16x32_bf16 v[64:67], v[216:219], v[200:203], v[64:67]
	v_mfma_f32_16x16x32_bf16 v[68:71], v[216:219], v[204:207], v[68:71]
	global_load_dwordx4 v[160:163], v58, s[8:9] offset:192
	v_mfma_f32_16x16x32_bf16 v[72:75], v[216:219], v[208:211], v[72:75]
	v_mfma_f32_16x16x32_bf16 v[76:79], v[216:219], v[212:215], v[76:79]
	global_load_dwordx4 v[164:167], v59, s[8:9] offset:192
	v_mfma_f32_16x16x32_bf16 v[80:83], v[220:223], v[200:203], v[80:83]
	v_mfma_f32_16x16x32_bf16 v[84:87], v[220:223], v[204:207], v[84:87]
	global_load_dwordx4 v[168:171], v56, s[8:9] offset:256
	v_mfma_f32_16x16x32_bf16 v[88:91], v[220:223], v[208:211], v[88:91]
	v_mfma_f32_16x16x32_bf16 v[92:95], v[220:223], v[212:215], v[92:95]
	global_load_dwordx4 v[172:175], v57, s[8:9] offset:256
	v_mfma_f32_16x16x32_bf16 v[96:99], v[224:227], v[200:203], v[96:99]
	v_mfma_f32_16x16x32_bf16 v[100:103], v[224:227], v[204:207], v[100:103]
	global_load_dwordx4 v[176:179], v58, s[8:9] offset:256
	v_mfma_f32_16x16x32_bf16 v[104:107], v[224:227], v[208:211], v[104:107]
	v_mfma_f32_16x16x32_bf16 v[108:111], v[224:227], v[212:215], v[108:111]
	global_load_dwordx4 v[180:183], v59, s[8:9] offset:256
	v_mfma_f32_16x16x32_bf16 v[112:115], v[228:231], v[200:203], v[112:115]
	v_mfma_f32_16x16x32_bf16 v[116:119], v[228:231], v[204:207], v[116:119]
	global_load_dwordx4 v[184:187], v56, s[8:9] offset:320
	v_mfma_f32_16x16x32_bf16 v[120:123], v[228:231], v[208:211], v[120:123]
	v_mfma_f32_16x16x32_bf16 v[124:127], v[228:231], v[212:215], v[124:127]
	global_load_dwordx4 v[188:191], v57, s[8:9] offset:320
	v_mfma_f32_16x16x32_bf16 v[128:131], v[232:235], v[200:203], v[128:131]
	v_mfma_f32_16x16x32_bf16 v[132:135], v[232:235], v[204:207], v[132:135]
	global_load_dwordx4 v[192:195], v58, s[8:9] offset:320
	v_mfma_f32_16x16x32_bf16 v[136:139], v[232:235], v[208:211], v[136:139]
	v_mfma_f32_16x16x32_bf16 v[140:143], v[232:235], v[212:215], v[140:143]
	global_load_dwordx4 v[196:199], v59, s[8:9] offset:320
	v_mfma_f32_16x16x32_bf16 v[144:147], v[236:239], v[200:203], v[144:147]
	v_mfma_f32_16x16x32_bf16 v[148:151], v[236:239], v[204:207], v[148:151]
	v_mfma_f32_16x16x32_bf16 v[152:155], v[236:239], v[208:211], v[152:155]
	v_mfma_f32_16x16x32_bf16 v[156:159], v[236:239], v[212:215], v[156:159]
	s_waitcnt vmcnt(23)
	v_pk_add_f32 v[64:65], v[64:65], v[16:17]
	v_pk_add_f32 v[66:67], v[66:67], v[18:19]
	global_store_dwordx4 v56, v[64:67], s[10:11] offset:0 sc0 sc1
	s_waitcnt vmcnt(23)
	v_pk_add_f32 v[68:69], v[68:69], v[20:21]
	v_pk_add_f32 v[70:71], v[70:71], v[22:23]
	global_store_dwordx4 v57, v[68:71], s[10:11] offset:0 sc0 sc1
	s_waitcnt vmcnt(23)
	v_pk_add_f32 v[72:73], v[72:73], v[24:25]
	v_pk_add_f32 v[74:75], v[74:75], v[26:27]
	global_store_dwordx4 v58, v[72:75], s[10:11] offset:0 sc0 sc1
	s_waitcnt vmcnt(23)
	v_pk_add_f32 v[76:77], v[76:77], v[28:29]
	v_pk_add_f32 v[78:79], v[78:79], v[30:31]
	global_store_dwordx4 v59, v[76:79], s[10:11] offset:0 sc0 sc1
	s_waitcnt vmcnt(23)
	v_pk_add_f32 v[80:81], v[80:81], v[32:33]
	v_pk_add_f32 v[82:83], v[82:83], v[34:35]
	global_store_dwordx4 v56, v[80:83], s[10:11] offset:64 sc0 sc1
	s_waitcnt vmcnt(23)
	v_pk_add_f32 v[84:85], v[84:85], v[36:37]
	v_pk_add_f32 v[86:87], v[86:87], v[38:39]
	global_store_dwordx4 v57, v[84:87], s[10:11] offset:64 sc0 sc1
	s_waitcnt vmcnt(23)
	v_pk_add_f32 v[88:89], v[88:89], v[40:41]
	v_pk_add_f32 v[90:91], v[90:91], v[42:43]
	global_store_dwordx4 v58, v[88:91], s[10:11] offset:64 sc0 sc1
	s_waitcnt vmcnt(23)
	v_pk_add_f32 v[92:93], v[92:93], v[44:45]
	v_pk_add_f32 v[94:95], v[94:95], v[46:47]
	global_store_dwordx4 v59, v[92:95], s[10:11] offset:64 sc0 sc1
	s_waitcnt vmcnt(23)
	v_pk_add_f32 v[96:97], v[96:97], v[48:49]
	v_pk_add_f32 v[98:99], v[98:99], v[50:51]
	global_store_dwordx4 v56, v[96:99], s[10:11] offset:128 sc0 sc1
	s_waitcnt vmcnt(23)
	v_pk_add_f32 v[100:101], v[100:101], v[52:53]
	v_pk_add_f32 v[102:103], v[102:103], v[54:55]
	global_store_dwordx4 v57, v[100:103], s[10:11] offset:128 sc0 sc1
	s_waitcnt vmcnt(23)
	v_pk_add_f32 v[104:105], v[104:105], v[240:241]
	v_pk_add_f32 v[106:107], v[106:107], v[242:243]
	global_store_dwordx4 v58, v[104:107], s[10:11] offset:128 sc0 sc1
	s_waitcnt vmcnt(23)
	v_pk_add_f32 v[108:109], v[108:109], v[244:245]
	v_pk_add_f32 v[110:111], v[110:111], v[246:247]
	global_store_dwordx4 v59, v[108:111], s[10:11] offset:128 sc0 sc1
	s_waitcnt vmcnt(23)
	v_pk_add_f32 v[112:113], v[112:113], v[248:249]
	v_pk_add_f32 v[114:115], v[114:115], v[250:251]
	global_store_dwordx4 v56, v[112:115], s[10:11] offset:192 sc0 sc1
	s_waitcnt vmcnt(23)
	v_pk_add_f32 v[116:117], v[116:117], v[252:253]
	v_pk_add_f32 v[118:119], v[118:119], v[254:255]
	global_store_dwordx4 v57, v[116:119], s[10:11] offset:192 sc0 sc1
	s_waitcnt vmcnt(23)
	v_pk_add_f32 v[120:121], v[120:121], v[160:161]
	v_pk_add_f32 v[122:123], v[122:123], v[162:163]
	global_store_dwordx4 v58, v[120:123], s[10:11] offset:192 sc0 sc1
	s_waitcnt vmcnt(23)
	v_pk_add_f32 v[124:125], v[124:125], v[164:165]
	v_pk_add_f32 v[126:127], v[126:127], v[166:167]
	global_store_dwordx4 v59, v[124:127], s[10:11] offset:192 sc0 sc1
	s_waitcnt vmcnt(23)
	v_pk_add_f32 v[128:129], v[128:129], v[168:169]
	v_pk_add_f32 v[130:131], v[130:131], v[170:171]
	global_store_dwordx4 v56, v[128:131], s[10:11] offset:256 sc0 sc1
	s_waitcnt vmcnt(23)
	v_pk_add_f32 v[132:133], v[132:133], v[172:173]
	v_pk_add_f32 v[134:135], v[134:135], v[174:175]
	global_store_dwordx4 v57, v[132:135], s[10:11] offset:256 sc0 sc1
	s_waitcnt vmcnt(23)
	v_pk_add_f32 v[136:137], v[136:137], v[176:177]
	v_pk_add_f32 v[138:139], v[138:139], v[178:179]
	global_store_dwordx4 v58, v[136:139], s[10:11] offset:256 sc0 sc1
	s_waitcnt vmcnt(23)
	v_pk_add_f32 v[140:141], v[140:141], v[180:181]
	v_pk_add_f32 v[142:143], v[142:143], v[182:183]
	global_store_dwordx4 v59, v[140:143], s[10:11] offset:256 sc0 sc1
	s_waitcnt vmcnt(23)
	v_pk_add_f32 v[144:145], v[144:145], v[184:185]
	v_pk_add_f32 v[146:147], v[146:147], v[186:187]
	global_store_dwordx4 v56, v[144:147], s[10:11] offset:320 sc0 sc1
	s_waitcnt vmcnt(23)
	v_pk_add_f32 v[148:149], v[148:149], v[188:189]
	v_pk_add_f32 v[150:151], v[150:151], v[190:191]
	global_store_dwordx4 v57, v[148:151], s[10:11] offset:320 sc0 sc1
	s_waitcnt vmcnt(23)
	v_pk_add_f32 v[152:153], v[152:153], v[192:193]
	v_pk_add_f32 v[154:155], v[154:155], v[194:195]
	global_store_dwordx4 v58, v[152:155], s[10:11] offset:320 sc0 sc1
	s_waitcnt vmcnt(23)
	v_pk_add_f32 v[156:157], v[156:157], v[196:197]
	v_pk_add_f32 v[158:159], v[158:159], v[198:199]
	global_store_dwordx4 v59, v[156:159], s[10:11] offset:320 sc0 sc1
